# GEMM3 routing tail: the coalesced expert-index / gate stores issued write-through (sc0 sc1) ahead of the GEMM3->U barrier
# baseline (speedup 1.0000x reference)
; #define PG8_LAS __attribute__((address_space(3)))
;     __device__ __forceinline__ void fused(f32x4 (&acc)[2][2][4][2], const Unit& u, int wr, int wc, int fr, int fq, PG8_LAS unsigned char* lds, int wid, int lane) const {
;     ...
;         if (half == 0) {
;             PG8_LAS int* idxl = (PG8_LAS int*)(lds + 65536) + row * 32;
;             float v0[16], v1[16];
; #pragma unroll
;             for (int q = 0; q < 16; ++q) { const unsigned b0 = __float_as_uint(top0[q]), b1 = __float_as_uint(top1[q]);
;                 v0[q] = __uint_as_float(b0 & ~127u); v1[q] = __uint_as_float(b1 & ~127u); idxl[q] = (int)(b0 & 127u); idxl[16 + q] = (int)(b1 & 127u); }
;             float best[16];
;             { float cv[16]; cv[0] = __uint_as_float((__float_as_uint(v0[0] + v1[0]) & ~255u) | 0u); cv[1] = __uint_as_float((__float_as_uint(v0[0] + v1[1]) & ~255u) | 1u); cv[2] = __uint_as_float((__float_as_uint(v0[0] + v1[2]) & ~255u) | 2u); cv[3] = __uint_as_float((__float_as_uint(v0[0] + v1[3]) & ~255u) | 3u); cv[4] = __uint_as_float((__float_as_uint(v0[0] + v1[4]) & ~255u) | 4u); cv[5] = __uint_as_float((__float_as_uint(v0[0] + v1[5]) & ~255u) | 5u); cv[6] = __uint_as_float((__float_as_uint(v0[0] + v1[6]) & ~255u) | 6u); cv[7] = __uint_as_float((__float_as_uint(v0[0] + v1[7]) & ~255u) | 7u); cv[8] = __uint_as_float((__float_as_uint(v0[0] + v1[8]) & ~255u) | 8u); cv[9] = __uint_as_float((__float_as_uint(v0[0] + v1[9]) & ~255u) | 9u); cv[10] = __uint_as_float((__float_as_uint(v0[0] + v1[10]) & ~255u) | 10u); cv[11] = __uint_as_float((__float_as_uint(v0[0] + v1[11]) & ~255u) | 11u); cv[12] = __uint_as_float((__float_as_uint(v0[0] + v1[12]) & ~255u) | 12u); cv[13] = __uint_as_float((__float_as_uint(v0[0] + v1[13]) & ~255u) | 13u); cv[14] = __uint_as_float((__float_as_uint(v0[0] + v1[14]) & ~255u) | 14u); cv[15] = __uint_as_float((__float_as_uint(v0[0] + v1[15]) & ~255u) | 15u); sort16_desc(cv);
; #pragma unroll
;               for (int q = 0; q < 16; ++q) best[q] = cv[q]; }
.LBB0_588:
	s_waitcnt lgkmcnt(0)
	s_barrier
	s_and_b64 vcc, exec, s[4:5]
	s_cbranch_vccnz .LBB0_590
	v_lshl_add_u32 v16, v128, 7, 0
	v_add_u32_e32 v16, 0x10000, v16
	v_and_b32_e32 v17, 0xffffff80, v12
	v_and_b32_e32 v18, 0xffffff80, v13
	v_and_b32_e32 v21, 0x7f, v77
	v_and_b32_e32 v20, 0x7f, v76
	v_and_b32_e32 v13, 0x7f, v13
	v_and_b32_e32 v12, 0x7f, v12
	v_and_b32_e32 v26, 0xffffff80, v14
	v_and_b32_e32 v28, 0xffffff80, v15
	v_and_b32_e32 v23, 0x7f, v79
	v_and_b32_e32 v22, 0x7f, v78
	v_and_b32_e32 v15, 0x7f, v15
	v_and_b32_e32 v14, 0x7f, v14
	ds_write_b128 v16, v[20:23]
	ds_write_b128 v16, v[12:15] offset:64
	v_and_b32_e32 v21, 0xffffff80, v8
	v_and_b32_e32 v23, 0xffffff80, v9
	v_and_b32_e32 v13, 0x7f, v73
	v_and_b32_e32 v12, 0x7f, v72
	v_and_b32_e32 v9, 0x7f, v9
	v_and_b32_e32 v8, 0x7f, v8
	v_and_b32_e32 v30, 0xffffff80, v10
	v_and_b32_e32 v32, 0xffffff80, v11
	v_and_b32_e32 v15, 0x7f, v75
	v_and_b32_e32 v14, 0x7f, v74
	v_and_b32_e32 v11, 0x7f, v11
	v_and_b32_e32 v10, 0x7f, v10
	v_and_b32_e32 v19, 0xffffff80, v76
	ds_write_b128 v16, v[12:15] offset:16
	ds_write_b128 v16, v[8:11] offset:80
	v_and_b32_e32 v13, 0xffffff80, v4
	v_and_b32_e32 v15, 0xffffff80, v5
	v_and_b32_e32 v9, 0x7f, v69
	v_and_b32_e32 v8, 0x7f, v68
	v_and_b32_e32 v5, 0x7f, v5
	v_and_b32_e32 v4, 0x7f, v4
	v_and_b32_e32 v34, 0xffffff80, v6
	v_and_b32_e32 v36, 0xffffff80, v7
	v_and_b32_e32 v11, 0x7f, v71
	v_and_b32_e32 v10, 0x7f, v70
	v_and_b32_e32 v7, 0x7f, v7
	v_and_b32_e32 v6, 0x7f, v6
	ds_write_b128 v16, v[8:11] offset:32
	ds_write_b128 v16, v[4:7] offset:96
	v_and_b32_e32 v5, 0x7f, v65
	v_and_b32_e32 v4, 0x7f, v64
	v_and_b32_e32 v41, 0xffffff80, v2
	v_and_b32_e32 v42, 0xffffff80, v3
	v_and_b32_e32 v7, 0x7f, v67
	v_and_b32_e32 v6, 0x7f, v66
	v_and_b32_e32 v11, 0x7f, v3
	v_and_b32_e32 v10, 0x7f, v2
	v_add_f32_e32 v2, v19, v17
	s_movk_i32 s4, 0xff00
	v_add_f32_e32 v3, v19, v18
	v_and_b32_e32 v24, 0xffffff80, v77
	ds_write_b128 v16, v[4:7] offset:48
	v_and_b32_e32 v2, 0xffffff00, v2
	v_and_or_b32 v3, v3, s4, 1
	v_add_f32_e32 v4, v19, v26
	v_add_f32_e32 v5, v19, v28
	v_and_b32_e32 v40, 0xffffff80, v1
	v_and_b32_e32 v9, 0x7f, v1
	v_and_b32_e32 v8, 0x7f, v0
	v_and_or_b32 v4, v4, s4, 2
	v_and_or_b32 v5, v5, s4, 3
	v_add_f32_e32 v48, v24, v17
	v_add_f32_e32 v49, v24, v18
	ds_write_b128 v16, v[8:11] offset:112
	v_add_f32_e32 v6, v19, v21
	v_add_f32_e32 v7, v19, v23
	v_add_f32_e32 v11, v19, v15
	v_add_f32_e32 v15, v19, v36
	v_add_f32_e32 v36, v19, v40
	v_max_f32_e32 v40, v2, v3
	v_min_f32_e32 v2, v2, v3
	v_max_f32_e32 v3, v5, v5
	v_and_or_b32 v48, v48, s4, 16
	v_and_or_b32 v49, v49, s4, 17
	v_add_f32_e32 v50, v24, v26
	v_add_f32_e32 v51, v24, v28
	v_and_or_b32 v6, v6, s4, 4
	v_and_or_b32 v7, v7, s4, 5
	v_add_f32_e32 v8, v19, v30
	v_add_f32_e32 v9, v19, v32
	v_max_f32_e32 v5, v4, v3
	v_min_f32_e32 v3, v4, v3
	v_and_or_b32 v50, v50, s4, 18
	v_and_or_b32 v51, v51, s4, 19
	v_and_or_b32 v8, v8, s4, 6
	v_and_or_b32 v9, v9, s4, 7
	v_max_f32_e32 v4, v40, v5
	v_min_f32_e32 v5, v40, v5
	v_max_f32_e32 v40, v2, v3
	v_add_f32_e32 v52, v24, v21
	v_add_f32_e32 v23, v24, v23
	v_add_f32_e32 v30, v24, v30
	v_add_f32_e32 v24, v24, v32
	v_max_f32_e32 v58, v48, v49
	v_min_f32_e32 v48, v48, v49
	v_max_f32_e32 v49, v51, v51
	v_min_f32_e32 v2, v2, v3
	v_max_f32_e32 v3, v40, v5
	v_min_f32_e32 v5, v40, v5
	v_max_f32_e32 v40, v6, v7
	v_min_f32_e32 v6, v6, v7
	v_max_f32_e32 v7, v9, v9
	v_and_or_b32 v52, v52, s4, 20
	v_and_or_b32 v23, v23, s4, 21
	v_and_or_b32 v30, v30, s4, 22
	v_and_or_b32 v24, v24, s4, 23
	v_max_f32_e32 v51, v50, v49
	v_min_f32_e32 v49, v50, v49
	v_max_f32_e32 v9, v8, v7
	v_min_f32_e32 v7, v8, v7
	v_max_f32_e32 v50, v58, v51
	v_min_f32_e32 v51, v58, v51
	v_max_f32_e32 v58, v48, v49
	v_max_f32_e32 v8, v40, v9
	v_min_f32_e32 v9, v40, v9
	v_max_f32_e32 v40, v6, v7
	v_min_f32_e32 v48, v48, v49
	v_max_f32_e32 v49, v58, v51
	v_min_f32_e32 v51, v58, v51
	v_max_f32_e32 v58, v52, v23
	v_min_f32_e32 v23, v52, v23
	v_max_f32_e32 v52, v30, v24
	v_min_f32_e32 v24, v30, v24
	v_min_f32_e32 v6, v6, v7
	v_max_f32_e32 v7, v40, v9
	v_min_f32_e32 v9, v40, v9
	v_max_f32_e32 v30, v58, v52
	v_min_f32_e32 v52, v58, v52
	v_max_f32_e32 v58, v23, v24
	v_max_f32_e32 v40, v4, v8
	v_min_f32_e32 v4, v4, v8
	v_max_f32_e32 v8, v5, v9
	v_min_f32_e32 v23, v23, v24
	v_max_f32_e32 v24, v58, v52
	v_min_f32_e32 v52, v58, v52
	v_and_b32_e32 v25, 0xffffff80, v78
	v_add_f32_e32 v10, v19, v13
	v_min_f32_e32 v5, v5, v9
	v_max_f32_e32 v9, v8, v4
	v_min_f32_e32 v4, v8, v4
	v_max_f32_e32 v8, v3, v7
	v_min_f32_e32 v3, v3, v7
	v_max_f32_e32 v7, v2, v6
	v_max_f32_e32 v58, v50, v30
	v_min_f32_e32 v30, v50, v30
	v_max_f32_e32 v50, v51, v52
	v_and_or_b32 v10, v10, s4, 8
	v_and_or_b32 v11, v11, s4, 9
	v_add_f32_e32 v13, v19, v34
	v_min_f32_e32 v2, v2, v6
	v_max_f32_e32 v6, v7, v3
	v_min_f32_e32 v3, v7, v3
	v_add_f32_e32 v32, v25, v17
	v_add_f32_e32 v53, v25, v18
	v_min_f32_e32 v51, v51, v52
	v_max_f32_e32 v52, v50, v30
	v_min_f32_e32 v30, v50, v30
	v_max_f32_e32 v50, v49, v24
	v_min_f32_e32 v24, v49, v24
	v_max_f32_e32 v49, v48, v23
	v_and_or_b32 v13, v13, s4, 10
	v_and_or_b32 v15, v15, s4, 11
	v_max_f32_e32 v7, v8, v9
	v_min_f32_e32 v8, v8, v9
	v_max_f32_e32 v9, v6, v4
	v_min_f32_e32 v4, v6, v4
	v_max_f32_e32 v6, v3, v5
	v_min_f32_e32 v3, v3, v5
	v_max_f32_e32 v5, v11, v11
	v_and_or_b32 v32, v32, s4, 32
	v_and_or_b32 v53, v53, s4, 33
	v_add_f32_e32 v54, v25, v26
	v_add_f32_e32 v55, v25, v28
	v_min_f32_e32 v23, v48, v23
	v_max_f32_e32 v48, v49, v24
	v_min_f32_e32 v24, v49, v24
	v_and_b32_e32 v27, 0xffffff80, v79
	v_and_b32_e32 v38, 0xffffff80, v0
	v_max_f32_e32 v11, v10, v5
	v_min_f32_e32 v5, v10, v5
	v_max_f32_e32 v10, v15, v15
;     __device__ __forceinline__ void fused(f32x4 (&acc)[2][2][4][2], const Unit& u, int wr, int wc, int fr, int fq, PG8_LAS unsigned char* lds, int wid, int lane) const {
;     ...
;             { float cv[16]; cv[0] = __uint_as_float((__float_as_uint(v0[0] + v1[0]) & ~255u) | 0u); cv[1] = __uint_as_float((__float_as_uint(v0[0] + v1[1]) & ~255u) | 1u); cv[2] = __uint_as_float((__float_as_uint(v0[0] + v1[2]) & ~255u) | 2u); cv[3] = __uint_as_float((__float_as_uint(v0[0] + v1[3]) & ~255u) | 3u); cv[4] = __uint_as_float((__float_as_uint(v0[0] + v1[4]) & ~255u) | 4u); cv[5] = __uint_as_float((__float_as_uint(v0[0] + v1[5]) & ~255u) | 5u); cv[6] = __uint_as_float((__float_as_uint(v0[0] + v1[6]) & ~255u) | 6u); cv[7] = __uint_as_float((__float_as_uint(v0[0] + v1[7]) & ~255u) | 7u); cv[8] = __uint_as_float((__float_as_uint(v0[0] + v1[8]) & ~255u) | 8u); cv[9] = __uint_as_float((__float_as_uint(v0[0] + v1[9]) & ~255u) | 9u); cv[10] = __uint_as_float((__float_as_uint(v0[0] + v1[10]) & ~255u) | 10u); cv[11] = __uint_as_float((__float_as_uint(v0[0] + v1[11]) & ~255u) | 11u); cv[12] = __uint_as_float((__float_as_uint(v0[0] + v1[12]) & ~255u) | 12u); cv[13] = __uint_as_float((__float_as_uint(v0[0] + v1[13]) & ~255u) | 13u); cv[14] = __uint_as_float((__float_as_uint(v0[0] + v1[14]) & ~255u) | 14u); cv[15] = __uint_as_float((__float_as_uint(v0[0] + v1[15]) & ~255u) | 15u); sort16_desc(cv);
; #pragma unroll
;               for (int q = 0; q < 16; ++q) best[q] = cv[q]; }
	v_and_or_b32 v54, v54, s4, 34
	v_and_or_b32 v55, v55, s4, 35
	v_max_f32_e32 v49, v50, v52
	v_min_f32_e32 v50, v50, v52
	v_max_f32_e32 v52, v48, v30
	v_min_f32_e32 v30, v48, v30
	v_max_f32_e32 v48, v24, v51
	v_min_f32_e32 v24, v24, v51
	v_max_f32_e32 v51, v53, v53
	v_add_f32_e32 v34, v19, v38
	v_max_f32_e32 v15, v13, v10
	v_min_f32_e32 v10, v13, v10
	v_add_f32_e32 v21, v25, v21
	v_add_f32_e32 v25, v27, v17
	v_max_f32_e32 v53, v32, v51
	v_min_f32_e32 v32, v32, v51
	v_max_f32_e32 v51, v55, v55
	v_and_or_b32 v34, v34, s4, 12
	v_and_or_b32 v36, v36, s4, 13
	v_add_f32_e32 v38, v19, v41
	v_add_f32_e32 v19, v19, v42
	v_max_f32_e32 v13, v11, v15
	v_min_f32_e32 v11, v11, v15
	v_max_f32_e32 v15, v5, v10
	v_and_or_b32 v21, v21, s4, 36
	v_and_or_b32 v25, v25, s4, 48
	v_add_f32_e32 v56, v27, v18
	v_add_f32_e32 v57, v27, v26
	v_max_f32_e32 v55, v54, v51
	v_min_f32_e32 v51, v54, v51
	v_and_or_b32 v38, v38, s4, 14
	v_and_or_b32 v19, v19, s4, 15
	v_min_f32_e32 v5, v5, v10
	v_max_f32_e32 v10, v15, v11
	v_min_f32_e32 v11, v15, v11
	v_max_f32_e32 v15, v36, v36
	v_and_or_b32 v56, v56, s4, 49
	v_and_or_b32 v57, v57, s4, 50
	v_max_f32_e32 v54, v53, v55
	v_min_f32_e32 v53, v53, v55
	v_max_f32_e32 v55, v32, v51
	v_max_f32_e32 v36, v34, v15
	v_min_f32_e32 v15, v34, v15
	v_max_f32_e32 v34, v38, v38
	v_min_f32_e32 v32, v32, v51
	v_max_f32_e32 v51, v55, v53
	v_min_f32_e32 v53, v55, v53
	v_max_f32_e32 v55, v21, v25
	v_min_f32_e32 v21, v21, v25
	v_max_f32_e32 v25, v57, v57
	v_max_f32_e32 v38, v34, v19
	v_min_f32_e32 v19, v34, v19
	v_max_f32_e32 v57, v56, v25
	v_min_f32_e32 v25, v56, v25
	v_max_f32_e32 v34, v36, v38
	v_min_f32_e32 v36, v36, v38
	v_max_f32_e32 v38, v15, v19
	v_max_f32_e32 v56, v55, v57
	v_min_f32_e32 v55, v55, v57
	v_max_f32_e32 v57, v21, v25
	v_min_f32_e32 v15, v15, v19
	v_max_f32_e32 v19, v38, v36
	v_min_f32_e32 v36, v38, v36
	v_min_f32_e32 v21, v21, v25
	v_max_f32_e32 v25, v57, v55
	v_min_f32_e32 v55, v57, v55
	v_max_f32_e32 v38, v13, v34
	v_min_f32_e32 v13, v13, v34
	v_max_f32_e32 v34, v11, v36
	v_max_f32_e32 v57, v54, v56
	v_min_f32_e32 v54, v54, v56
	v_max_f32_e32 v56, v53, v55
	v_min_f32_e32 v11, v11, v36
	v_max_f32_e32 v36, v34, v13
	v_min_f32_e32 v13, v34, v13
	v_max_f32_e32 v34, v10, v19
	v_min_f32_e32 v10, v10, v19
	v_max_f32_e32 v19, v5, v15
	v_min_f32_e32 v53, v53, v55
	v_max_f32_e32 v55, v56, v54
	v_min_f32_e32 v54, v56, v54
	v_max_f32_e32 v56, v51, v25
	v_min_f32_e32 v25, v51, v25
	v_max_f32_e32 v51, v32, v21
	v_min_f32_e32 v5, v5, v15
	v_max_f32_e32 v15, v19, v10
	v_min_f32_e32 v21, v32, v21
	v_max_f32_e32 v32, v51, v25
	v_min_f32_e32 v10, v19, v10
	v_max_f32_e32 v19, v34, v36
	v_min_f32_e32 v34, v34, v36
	v_max_f32_e32 v36, v15, v13
	v_min_f32_e32 v13, v15, v13
	v_min_f32_e32 v25, v51, v25
	v_max_f32_e32 v51, v56, v55
	v_min_f32_e32 v55, v56, v55
	v_max_f32_e32 v56, v32, v54
	v_min_f32_e32 v32, v32, v54
	v_max_f32_e32 v15, v10, v11
	v_min_f32_e32 v10, v10, v11
	v_min_f32_e32 v11, v40, v38
	v_max_f32_e32 v41, v4, v13
	v_max_f32_e32 v54, v25, v53
	v_min_f32_e32 v25, v25, v53
	v_min_f32_e32 v53, v58, v57
	v_max_f32_e32 v59, v30, v32
	v_min_f32_e32 v4, v4, v13
	v_max_f32_e32 v13, v41, v11
	v_min_f32_e32 v11, v41, v11
	v_max_f32_e32 v41, v8, v34
	v_min_f32_e32 v8, v8, v34
	v_max_f32_e32 v34, v3, v10
	v_min_f32_e32 v30, v30, v32
	v_max_f32_e32 v32, v59, v53
	v_min_f32_e32 v53, v59, v53
	v_max_f32_e32 v59, v50, v55
	v_min_f32_e32 v50, v50, v55
	v_max_f32_e32 v55, v24, v25
	v_min_f32_e32 v3, v3, v10
	v_max_f32_e32 v10, v34, v8
	v_min_f32_e32 v8, v34, v8
	v_min_f32_e32 v24, v24, v25
	v_max_f32_e32 v25, v55, v50
	v_min_f32_e32 v50, v55, v50
	v_max_f32_e32 v34, v41, v13
	v_min_f32_e32 v13, v41, v13
	v_max_f32_e32 v41, v10, v11
	v_min_f32_e32 v10, v10, v11
	v_max_f32_e32 v11, v8, v4
	v_min_f32_e32 v4, v8, v4
	v_max_f32_e32 v8, v7, v19
	v_min_f32_e32 v7, v7, v19
	v_max_f32_e32 v19, v6, v15
	v_max_f32_e32 v55, v59, v32
	v_min_f32_e32 v32, v59, v32
	v_max_f32_e32 v59, v25, v53
	v_min_f32_e32 v25, v25, v53
	v_max_f32_e32 v53, v50, v30
	v_min_f32_e32 v30, v50, v30
	v_max_f32_e32 v50, v49, v51
	v_min_f32_e32 v49, v49, v51
	v_max_f32_e32 v51, v48, v54
	v_min_f32_e32 v6, v6, v15
	v_max_f32_e32 v15, v19, v7
	v_min_f32_e32 v7, v19, v7
	v_max_f32_e32 v19, v9, v36
	v_min_f32_e32 v9, v9, v36
	v_max_f32_e32 v36, v2, v5
	v_min_f32_e32 v48, v48, v54
	v_max_f32_e32 v54, v51, v49
	v_min_f32_e32 v49, v51, v49
	v_max_f32_e32 v51, v52, v56
	v_min_f32_e32 v52, v52, v56
	v_max_f32_e32 v56, v23, v21
	v_min_f32_e32 v2, v2, v5
	v_max_f32_e32 v5, v36, v9
	v_min_f32_e32 v9, v36, v9
	v_max_f32_e32 v36, v19, v15
	v_min_f32_e32 v21, v23, v21
	v_max_f32_e32 v23, v56, v52
	v_min_f32_e32 v52, v56, v52
	v_and_b32_e32 v20, 0xffffff80, v72
	v_min_f32_e32 v15, v19, v15
	v_max_f32_e32 v19, v5, v7
	v_min_f32_e32 v5, v5, v7
	v_max_f32_e32 v7, v9, v6
	v_min_f32_e32 v6, v9, v6
	v_min_f32_e32 v9, v8, v34
	v_min_f32_e32 v42, v36, v13
	v_max_f32_e32 v56, v51, v54
	v_min_f32_e32 v51, v51, v54
	v_max_f32_e32 v54, v23, v49
	v_min_f32_e32 v23, v23, v49
	v_max_f32_e32 v49, v52, v48
	v_min_f32_e32 v48, v52, v48
	v_and_b32_e32 v39, 0xffffff80, v65
	v_min_f32_e32 v65, v48, v24
	v_max3_f32 v9, v9, v48, v24
	v_max3_f32 v24, v42, v49, v30
	v_add_f32_e32 v27, v27, v28
	v_add_f32_e32 v28, v20, v17
	v_add_f32_e32 v42, v20, v18
	v_add_f32_e32 v20, v20, v26
	v_and_b32_e32 v22, 0xffffff80, v73
	v_and_or_b32 v27, v27, s4, 51
	v_and_or_b32 v28, v28, s4, 64
	v_and_b32_e32 v42, 0xffffff00, v42
	v_and_b32_e32 v20, 0xffffff00, v20
	v_and_b32_e32 v29, 0xffffff80, v74
	v_and_b32_e32 v31, 0xffffff80, v75
	v_and_b32_e32 v33, 0xffffff80, v70
	v_and_b32_e32 v35, 0xffffff80, v71
	v_and_b32_e32 v37, 0xffffff80, v64
; __device__ __forceinline__ void sort16_desc(float (&v)[16]) {
;     CE(v[0], v[1]); CE(v[2], v[3]); CE(v[0], v[2]); CE(v[1], v[3]);
;     CE(v[1], v[2]); CE(v[4], v[5]); CE(v[6], v[7]); CE(v[4], v[6]);
;     CE(v[5], v[7]); CE(v[5], v[6]); CE(v[0], v[4]); CE(v[2], v[6]);
;     CE(v[2], v[4]); CE(v[1], v[5]); CE(v[3], v[7]); CE(v[3], v[5]);
;     CE(v[1], v[2]); CE(v[3], v[4]); CE(v[5], v[6]); CE(v[8], v[9]);
;     __device__ __forceinline__ void fused(f32x4 (&acc)[2][2][4][2], const Unit& u, int wr, int wc, int fr, int fq, PG8_LAS unsigned char* lds, int wid, int lane) const {
;     ...
;             { float cv[16]; cv[0] = __uint_as_float((__float_as_uint(v0[3] + v1[3]) & ~255u) | 51u); cv[1] = __uint_as_float((__float_as_uint(v0[4] + v1[0]) & ~255u) | 64u); cv[2] = __uint_as_float((__float_as_uint(v0[4] + v1[1]) & ~255u) | 65u); cv[3] = __uint_as_float((__float_as_uint(v0[4] + v1[2]) & ~255u) | 66u); cv[4] = __uint_as_float((__float_as_uint(v0[5] + v1[0]) & ~255u) | 80u); cv[5] = __uint_as_float((__float_as_uint(v0[5] + v1[1]) & ~255u) | 81u); cv[6] = __uint_as_float((__float_as_uint(v0[6] + v1[0]) & ~255u) | 96u); cv[7] = __uint_as_float((__float_as_uint(v0[6] + v1[1]) & ~255u) | 97u); cv[8] = __uint_as_float((__float_as_uint(v0[7] + v1[0]) & ~255u) | 112u); cv[9] = __uint_as_float((__float_as_uint(v0[7] + v1[1]) & ~255u) | 113u); cv[10] = __uint_as_float((__float_as_uint(v0[8] + v1[0]) & ~255u) | 128u); cv[11] = __uint_as_float((__float_as_uint(v0[9] + v1[0]) & ~255u) | 144u); cv[12] = __uint_as_float((__float_as_uint(v0[10] + v1[0]) & ~255u) | 160u); cv[13] = __uint_as_float((__float_as_uint(v0[11] + v1[0]) & ~255u) | 176u); cv[14] = __uint_as_float((__float_as_uint(v0[12] + v1[0]) & ~255u) | 192u); cv[15] = __uint_as_float((__float_as_uint(v0[13] + v1[0]) & ~255u) | 208u); sort16_desc(cv); merge_top16(best, cv); }
;             { float cv[16]; cv[0] = __uint_as_float((__float_as_uint(v0[14] + v1[0]) & ~255u) | 224u); cv[1] = __uint_as_float((__float_as_uint(v0[15] + v1[0]) & ~255u) | 240u); cv[2] = -INFINITY; cv[3] = -INFINITY; cv[4] = -INFINITY; cv[5] = -INFINITY; cv[6] = -INFINITY; cv[7] = -INFINITY; cv[8] = -INFINITY; cv[9] = -INFINITY; cv[10] = -INFINITY; cv[11] = -INFINITY; cv[12] = -INFINITY; cv[13] = -INFINITY; cv[14] = -INFINITY; cv[15] = -INFINITY; sort16_desc(cv); merge_top16(best, cv); }
	v_min_f32_e32 v43, v15, v41
	v_min_f32_e32 v44, v19, v10
	v_min_f32_e32 v62, v54, v25
	v_or_b32_e32 v42, 0x41, v42
	v_or_b32_e32 v20, 0x42, v20
	v_add_f32_e32 v26, v22, v17
	v_add_f32_e32 v22, v22, v18
	v_min_f32_e32 v63, v23, v53
	v_max3_f32 v23, v43, v23, v53
	v_max3_f32 v10, v19, v10, v62
	v_max3_f32 v19, v44, v54, v25
	v_and_b32_e32 v26, 0xffffff00, v26
	v_and_b32_e32 v22, 0xffffff00, v22
	v_add_f32_e32 v43, v29, v17
	v_add_f32_e32 v29, v29, v18
	v_add_f32_e32 v44, v31, v17
	v_add_f32_e32 v18, v31, v18
	v_add_f32_e32 v31, v33, v17
	v_add_f32_e32 v33, v35, v17
	v_add_f32_e32 v35, v37, v17
	v_add_f32_e32 v37, v39, v17
	v_max_f32_e32 v39, v27, v28
	v_min_f32_e32 v27, v27, v28
	v_max_f32_e32 v28, v42, v42
	v_or_b32_e32 v26, 0x50, v26
	v_or_b32_e32 v22, 0x51, v22
	v_and_b32_e32 v43, 0xffffff00, v43
	v_and_b32_e32 v29, 0xffffff00, v29
	v_max_f32_e32 v42, v28, v20
	v_min_f32_e32 v20, v28, v20
	v_or_b32_e32 v43, 0x60, v43
	v_or_b32_e32 v29, 0x61, v29
	v_max_f32_e32 v28, v39, v42
	v_min_f32_e32 v39, v39, v42
	v_max_f32_e32 v42, v27, v20
	v_min_f32_e32 v20, v27, v20
	v_max_f32_e32 v27, v42, v39
	v_min_f32_e32 v39, v42, v39
	v_max_f32_e32 v42, v26, v22
	v_min_f32_e32 v22, v26, v22
	v_max_f32_e32 v26, v29, v29
	v_max_f32_e32 v29, v43, v43
	v_max_f32_e32 v43, v29, v26
	v_min_f32_e32 v26, v29, v26
	v_max_f32_e32 v29, v42, v43
	v_min_f32_e32 v42, v42, v43
	v_max_f32_e32 v43, v22, v26
	v_and_b32_e32 v12, 0xffffff80, v68
	v_and_b32_e32 v14, 0xffffff80, v69
	v_min_f32_e32 v22, v22, v26
	v_max_f32_e32 v26, v43, v42
	v_min_f32_e32 v42, v43, v42
	v_add_f32_e32 v12, v12, v17
	v_add_f32_e32 v14, v14, v17
	v_max_f32_e32 v43, v28, v29
	v_min_f32_e32 v28, v28, v29
	v_max_f32_e32 v29, v39, v42
	v_and_b32_e32 v44, 0xffffff00, v44
	v_and_b32_e32 v18, 0xffffff00, v18
	v_and_b32_e32 v12, 0xffffff00, v12
	v_and_b32_e32 v14, 0xffffff00, v14
	v_min_f32_e32 v39, v39, v42
	v_max_f32_e32 v42, v29, v28
	v_min_f32_e32 v28, v29, v28
	v_max_f32_e32 v29, v27, v26
	v_min_f32_e32 v26, v27, v26
	v_max_f32_e32 v27, v20, v22
	v_or_b32_e32 v44, 0x70, v44
	v_or_b32_e32 v18, 0x71, v18
	v_or_b32_e32 v12, 0x80, v12
	v_or_b32_e32 v14, 0x90, v14
	v_min_f32_e32 v20, v20, v22
	v_max_f32_e32 v22, v27, v26
	v_min_f32_e32 v26, v27, v26
	v_and_b32_e32 v31, 0xffffff00, v31
	v_and_b32_e32 v33, 0xffffff00, v33
	v_max_f32_e32 v27, v29, v42
	v_min_f32_e32 v29, v29, v42
	v_max_f32_e32 v42, v22, v28
	v_min_f32_e32 v22, v22, v28
	v_max_f32_e32 v28, v26, v39
	v_min_f32_e32 v26, v26, v39
	v_max_f32_e32 v39, v44, v44
	v_or_b32_e32 v31, 0xa0, v31
	v_or_b32_e32 v33, 0xb0, v33
	v_and_b32_e32 v35, 0xffffff00, v35
	v_and_b32_e32 v37, 0xffffff00, v37
	v_max_f32_e32 v44, v39, v18
	v_min_f32_e32 v18, v39, v18
	v_max_f32_e32 v39, v12, v14
	v_min_f32_e32 v12, v12, v14
	v_or_b32_e32 v35, 0xc0, v35
	v_or_b32_e32 v37, 0xd0, v37
	v_max_f32_e32 v14, v44, v39
	v_min_f32_e32 v39, v44, v39
	v_max_f32_e32 v44, v18, v12
	v_min_f32_e32 v12, v18, v12
	v_max_f32_e32 v18, v44, v39
	v_min_f32_e32 v39, v44, v39
	v_max_f32_e32 v44, v31, v33
	v_min_f32_e32 v31, v31, v33
	v_max_f32_e32 v33, v37, v37
	v_max_f32_e32 v37, v35, v33
	v_min_f32_e32 v33, v35, v33
	v_max_f32_e32 v35, v44, v37
	v_min_f32_e32 v37, v44, v37
	v_max_f32_e32 v44, v31, v33
	v_min_f32_e32 v31, v31, v33
	v_max_f32_e32 v33, v44, v37
	v_min_f32_e32 v37, v44, v37
	v_max_f32_e32 v44, v14, v35
	v_min_f32_e32 v14, v14, v35
	v_max_f32_e32 v35, v39, v37
	v_min_f32_e32 v37, v39, v37
	v_max_f32_e32 v39, v35, v14
	v_min_f32_e32 v14, v35, v14
	v_max_f32_e32 v35, v18, v33
	v_min_f32_e32 v18, v18, v33
	v_max_f32_e32 v33, v12, v31
	v_min_f32_e32 v12, v12, v31
	v_max_f32_e32 v31, v33, v18
	v_min_f32_e32 v45, v5, v11
	v_min_f32_e32 v61, v51, v59
	v_min_f32_e32 v18, v33, v18
	v_max_f32_e32 v33, v35, v39
	v_min_f32_e32 v35, v35, v39
	v_max_f32_e32 v39, v31, v14
	v_min_f32_e32 v14, v31, v14
	v_max3_f32 v5, v5, v11, v61
	v_max3_f32 v11, v45, v51, v59
	v_max_f32_e32 v31, v18, v37
	v_min_f32_e32 v18, v18, v37
	v_min_f32_e32 v37, v43, v44
	v_max_f32_e32 v45, v22, v14
	v_min_f32_e32 v14, v22, v14
	v_max_f32_e32 v22, v45, v37
	v_min_f32_e32 v37, v45, v37
	v_max_f32_e32 v45, v29, v35
	v_min_f32_e32 v29, v29, v35
	v_max_f32_e32 v35, v26, v18
	v_min_f32_e32 v46, v7, v4
	v_min_f32_e32 v47, v6, v3
	v_min_f32_e32 v52, v50, v55
	v_min_f32_e32 v60, v56, v32
	v_min_f32_e32 v64, v49, v30
	v_min_f32_e32 v18, v26, v18
	v_max_f32_e32 v26, v35, v29
	v_min_f32_e32 v29, v35, v29
	v_max3_f32 v21, v40, v38, v21
	v_max3_f32 v8, v8, v34, v65
	v_max3_f32 v13, v36, v13, v64
	v_max3_f32 v15, v15, v41, v63
	v_max3_f32 v4, v7, v4, v60
	v_max3_f32 v7, v46, v56, v32
	v_max3_f32 v3, v6, v3, v52
	v_max3_f32 v6, v47, v50, v55
	v_max3_f32 v2, v2, v58, v57
	v_max_f32_e32 v35, v45, v22
	v_min_f32_e32 v22, v45, v22
	v_max_f32_e32 v45, v26, v37
	v_min_f32_e32 v26, v26, v37
	v_max_f32_e32 v37, v29, v14
	v_min_f32_e32 v14, v29, v14
	v_max_f32_e32 v29, v27, v33
	v_min_f32_e32 v27, v27, v33
	v_max_f32_e32 v33, v28, v31
	v_max_f32_e32 v25, v21, v19
	v_min_f32_e32 v19, v21, v19
	v_max_f32_e32 v21, v8, v5
	v_min_f32_e32 v5, v8, v5
	v_max_f32_e32 v8, v9, v11
	v_min_f32_e32 v9, v9, v11
	v_max_f32_e32 v11, v13, v4
	v_min_f32_e32 v4, v13, v4
	v_max_f32_e32 v13, v24, v7
	v_min_f32_e32 v7, v24, v7
	v_max_f32_e32 v24, v15, v3
	v_min_f32_e32 v3, v15, v3
	v_max_f32_e32 v15, v23, v6
	v_min_f32_e32 v6, v23, v6
	v_max_f32_e32 v23, v10, v2
	v_min_f32_e32 v2, v10, v2
	v_min_f32_e32 v28, v28, v31
	v_max_f32_e32 v31, v33, v27
	v_min_f32_e32 v27, v33, v27
	v_max_f32_e32 v33, v42, v39
	v_min_f32_e32 v39, v42, v39
	v_max_f32_e32 v42, v20, v12
	v_max_f32_e32 v10, v25, v13
	v_min_f32_e32 v13, v25, v13
	v_max_f32_e32 v25, v21, v24
	v_min_f32_e32 v21, v21, v24
;     __device__ __forceinline__ void fused(f32x4 (&acc)[2][2][4][2], const Unit& u, int wr, int wc, int fr, int fq, PG8_LAS unsigned char* lds, int wid, int lane) const {
;     ...
;             { float cv[16]; cv[0] = __uint_as_float((__float_as_uint(v0[14] + v1[0]) & ~255u) | 224u); cv[1] = __uint_as_float((__float_as_uint(v0[15] + v1[0]) & ~255u) | 240u); cv[2] = -INFINITY; cv[3] = -INFINITY; cv[4] = -INFINITY; cv[5] = -INFINITY; cv[6] = -INFINITY; cv[7] = -INFINITY; cv[8] = -INFINITY; cv[9] = -INFINITY; cv[10] = -INFINITY; cv[11] = -INFINITY; cv[12] = -INFINITY; cv[13] = -INFINITY; cv[14] = -INFINITY; cv[15] = -INFINITY; sort16_desc(cv); merge_top16(best, cv); }
;             float sc[16], sum = 0.f;
; #pragma unroll
;             for (int q = 0; q < 16; ++q) { sc[q] = __uint_as_float(__float_as_uint(best[q]) & ~255u); }
;             const float smax = sc[0];
; #pragma unroll
;             for (int q = 0; q < 16; ++q) { sc[q] = __builtin_amdgcn_exp2f((sc[q] - smax) * 1.4426950408889634f); }
; #pragma unroll
;             for (int q = 0; q < 16; ++q) sum += sc[q];
;             const float rs = 1.0f / sum;
;             asm volatile("s_waitcnt lgkmcnt(0)" ::: "memory");
;             int ex[16];
; #pragma unroll
;             for (int q = 0; q < 16; ++q) { const unsigned cid = __float_as_uint(best[q]) & 255u; ex[q] = idxl[cid >> 4] * 128 + idxl[16 + (cid & 15u)]; }
	v_max_f32_e32 v24, v8, v15
	v_min_f32_e32 v8, v8, v15
	v_max_f32_e32 v15, v11, v23
	v_min_f32_e32 v11, v11, v23
	v_max_f32_e32 v23, v19, v7
	v_min_f32_e32 v7, v19, v7
	v_max_f32_e32 v19, v5, v3
	v_min_f32_e32 v3, v5, v3
	v_max_f32_e32 v5, v9, v6
	v_min_f32_e32 v6, v9, v6
	v_max_f32_e32 v9, v4, v2
	v_min_f32_e32 v2, v4, v2
	v_min_f32_e32 v12, v20, v12
	v_max_f32_e32 v20, v42, v39
	v_min_f32_e32 v39, v42, v39
	v_and_b32_e32 v1, 0xffffff80, v66
	v_and_b32_e32 v0, 0xffffff80, v67
	v_max_f32_e32 v4, v10, v24
	v_min_f32_e32 v10, v10, v24
	v_max_f32_e32 v24, v25, v15
	v_min_f32_e32 v15, v25, v15
	v_max_f32_e32 v25, v13, v8
	v_min_f32_e32 v8, v13, v8
	v_max_f32_e32 v13, v21, v11
	v_min_f32_e32 v11, v21, v11
	v_max_f32_e32 v21, v23, v5
	v_min_f32_e32 v5, v23, v5
	v_max_f32_e32 v23, v19, v9
	v_min_f32_e32 v9, v19, v9
	v_max_f32_e32 v19, v7, v6
	v_min_f32_e32 v6, v7, v6
	v_max_f32_e32 v7, v3, v2
	v_min_f32_e32 v2, v3, v2
	v_max_f32_e32 v42, v33, v31
	v_min_f32_e32 v31, v33, v31
	v_max_f32_e32 v33, v20, v27
	v_min_f32_e32 v20, v20, v27
	v_max_f32_e32 v27, v39, v28
	v_min_f32_e32 v28, v39, v28
	v_min_f32_e32 v3, v4, v24
	v_min_f32_e32 v30, v10, v15
	v_min_f32_e32 v32, v25, v13
	v_min_f32_e32 v34, v8, v11
	v_min_f32_e32 v36, v21, v23
	v_min_f32_e32 v38, v5, v9
	v_min_f32_e32 v40, v19, v7
	v_min_f32_e32 v41, v6, v2
	v_max_f32_e32 v39, v29, v35
	v_min_f32_e32 v29, v29, v35
	v_max_f32_e32 v35, v42, v22
	v_min_f32_e32 v22, v42, v22
	v_max_f32_e32 v42, v31, v45
	v_min_f32_e32 v31, v31, v45
	v_max_f32_e32 v45, v33, v26
	v_min_f32_e32 v26, v33, v26
	v_max_f32_e32 v33, v20, v37
	v_min_f32_e32 v20, v20, v37
	v_max_f32_e32 v37, v27, v14
	v_min_f32_e32 v14, v27, v14
	v_max_f32_e32 v27, v28, v18
	v_min_f32_e32 v18, v28, v18
	v_add_f32_e32 v1, v1, v17
	v_add_f32_e32 v0, v0, v17
	v_max3_f32 v4, v4, v24, v12
	v_max_f32_e32 v3, v3, v18
	v_max3_f32 v10, v10, v15, v27
	v_max_f32_e32 v12, v30, v14
	v_max3_f32 v13, v25, v13, v37
	v_max_f32_e32 v14, v32, v20
	v_max3_f32 v8, v8, v11, v33
	v_max_f32_e32 v11, v34, v26
	v_max3_f32 v15, v21, v23, v45
	v_max_f32_e32 v18, v36, v31
	v_max3_f32 v5, v5, v9, v42
	v_max_f32_e32 v9, v38, v22
	v_max3_f32 v7, v19, v7, v35
	v_max_f32_e32 v19, v40, v29
	v_max3_f32 v2, v6, v2, v39
	v_max3_f32 v6, v41, v43, v44
	v_and_b32_e32 v1, 0xffffff00, v1
	v_and_b32_e32 v0, 0xffffff00, v0
	v_max_f32_e32 v20, v4, v15
	v_min_f32_e32 v4, v4, v15
	v_max_f32_e32 v15, v3, v18
	v_min_f32_e32 v3, v3, v18
	v_max_f32_e32 v18, v10, v5
	v_min_f32_e32 v5, v10, v5
	v_max_f32_e32 v10, v12, v9
	v_min_f32_e32 v9, v12, v9
	v_max_f32_e32 v12, v13, v7
	v_min_f32_e32 v7, v13, v7
	v_max_f32_e32 v13, v14, v19
	v_min_f32_e32 v14, v14, v19
	v_max_f32_e32 v19, v8, v2
	v_min_f32_e32 v2, v8, v2
	v_max_f32_e32 v8, v11, v6
	v_min_f32_e32 v6, v11, v6
	v_or_b32_e32 v1, 0xe0, v1
	v_or_b32_e32 v0, 0xf0, v0
	v_max_f32_e32 v11, v20, v12
	v_min_f32_e32 v12, v20, v12
	v_max_f32_e32 v20, v15, v13
	v_min_f32_e32 v13, v15, v13
	v_max_f32_e32 v15, v18, v19
	v_min_f32_e32 v18, v18, v19
	v_max_f32_e32 v19, v10, v8
	v_min_f32_e32 v8, v10, v8
	v_max_f32_e32 v10, v4, v7
	v_min_f32_e32 v4, v4, v7
	v_max_f32_e32 v7, v3, v14
	v_min_f32_e32 v3, v3, v14
	v_max_f32_e32 v14, v5, v2
	v_min_f32_e32 v2, v5, v2
	v_max_f32_e32 v5, v9, v6
	v_min_f32_e32 v6, v9, v6
	v_max_f32_e32 v9, v11, v15
	v_min_f32_e32 v11, v11, v15
	v_max_f32_e32 v15, v20, v19
	v_min_f32_e32 v19, v20, v19
	v_max_f32_e32 v20, v12, v18
	v_min_f32_e32 v12, v12, v18
	v_max_f32_e32 v18, v13, v8
	v_min_f32_e32 v8, v13, v8
	v_max_f32_e32 v13, v10, v14
	v_min_f32_e32 v10, v10, v14
	v_max_f32_e32 v14, v7, v5
	v_min_f32_e32 v5, v7, v5
	v_max_f32_e32 v7, v4, v2
	v_min_f32_e32 v2, v4, v2
	v_max_f32_e32 v4, v3, v6
	v_min_f32_e32 v3, v3, v6
	v_max_f32_e32 v17, v1, v0
	v_min_f32_e32 v0, v1, v0
	v_min_f32_e32 v6, v9, v15
	v_min_f32_e32 v21, v11, v19
	v_min_f32_e32 v22, v20, v18
	v_min_f32_e32 v23, v12, v8
	v_min_f32_e32 v24, v13, v14
	v_min_f32_e32 v25, v10, v5
	v_min_f32_e32 v26, v7, v4
	v_min_f32_e32 v27, v2, v3
	s_mov_b32 s4, 0xff800000
	v_max_f32_e32 v0, 0xff800000, v0
	v_max3_f32 v1, v9, v15, s4
	v_max_f32_e32 v6, 0xff800000, v6
	v_max3_f32 v9, v11, v19, s4
	v_max_f32_e32 v11, 0xff800000, v21
	v_max3_f32 v15, v20, v18, s4
	v_max_f32_e32 v18, 0xff800000, v22
	v_max3_f32 v8, v12, v8, s4
	v_max_f32_e32 v12, 0xff800000, v23
	v_max3_f32 v13, v13, v14, s4
	v_max_f32_e32 v14, 0xff800000, v24
	v_max3_f32 v5, v10, v5, s4
	v_max_f32_e32 v10, 0xff800000, v25
	v_max3_f32 v4, v7, v4, s4
	v_max_f32_e32 v7, 0xff800000, v26
	v_max3_f32 v0, v2, v3, v0
	v_max3_f32 v2, v27, v17, s4
	v_max_f32_e32 v3, v1, v13
	v_min_f32_e32 v1, v1, v13
	v_max_f32_e32 v13, v6, v14
	v_min_f32_e32 v6, v6, v14
	v_max_f32_e32 v14, v9, v5
	v_min_f32_e32 v5, v9, v5
	v_max_f32_e32 v9, v11, v10
	v_min_f32_e32 v10, v11, v10
	v_max_f32_e32 v11, v15, v4
	v_min_f32_e32 v4, v15, v4
	v_max_f32_e32 v15, v18, v7
	v_max_f32_e32 v17, v8, v0
	v_min_f32_e32 v0, v8, v0
	v_max_f32_e32 v8, v12, v2
	v_min_f32_e32 v2, v12, v2
	v_max_f32_e32 v12, v3, v11
	v_min_f32_e32 v3, v3, v11
	v_max_f32_e32 v11, v13, v15
	v_min_f32_e32 v13, v13, v15
	v_max_f32_e32 v15, v14, v17
	v_min_f32_e32 v14, v14, v17
	v_max_f32_e32 v17, v9, v8
	v_min_f32_e32 v8, v9, v8
	v_max_f32_e32 v9, v1, v4
	v_min_f32_e32 v24, v1, v4
	v_max_f32_e32 v27, v5, v0
	v_min_f32_e32 v28, v5, v0
	v_max_f32_e32 v29, v10, v2
	v_min_f32_e32 v30, v10, v2
	v_max_f32_e32 v0, v12, v15
	v_min_f32_e32 v1, v12, v15
	v_max_f32_e32 v2, v11, v17
	v_min_f32_e32 v4, v11, v17
	v_min_f32_e32 v7, v18, v7
	v_max_f32_e32 v33, v0, v2
	v_min_f32_e32 v34, v0, v2
	v_min_f32_e32 v36, v1, v4
	v_max_f32_e32 v25, v6, v7
	v_min_f32_e32 v26, v6, v7
	v_max_f32_e32 v35, v1, v4
	v_lshrrev_b32_e32 v0, 2, v33
	v_lshrrev_b32_e32 v2, 2, v34
	v_lshrrev_b32_e32 v6, 2, v36
	v_max_f32_e32 v17, v3, v14
	v_min_f32_e32 v31, v3, v14
	v_and_b32_e32 v0, 60, v0
	v_and_b32_e32 v1, 15, v33
	v_and_b32_e32 v2, 60, v2
	v_and_b32_e32 v3, 15, v34
	v_lshrrev_b32_e32 v4, 2, v35
	v_and_b32_e32 v5, 15, v35
	v_and_b32_e32 v6, 60, v6
	v_and_b32_e32 v7, 15, v36
	s_waitcnt lgkmcnt(0)
; #define RT_PK(q_) (ex[q_] | (int)((__float_as_uint(usc[ex[q_]]) >> 23) << 14))
;     __device__ __forceinline__ void fused(f32x4 (&acc)[2][2][4][2], const Unit& u, int wr, int wc, int fr, int fq, PG8_LAS unsigned char* lds, int wid, int lane) const {
;     ...
;             for (int q = 0; q < 16; ++q) { sc[q] = __uint_as_float(__float_as_uint(best[q]) & ~255u); }
;             const float smax = sc[0];
; #pragma unroll
;             for (int q = 0; q < 16; ++q) { sc[q] = __builtin_amdgcn_exp2f((sc[q] - smax) * 1.4426950408889634f); }
; #pragma unroll
;             for (int q = 0; q < 16; ++q) sum += sc[q];
;             const float rs = 1.0f / sum;
;             asm volatile("s_waitcnt lgkmcnt(0)" ::: "memory");
;             int ex[16];
; #pragma unroll
;             for (int q = 0; q < 16; ++q) { const unsigned cid = __float_as_uint(best[q]) & 255u; ex[q] = idxl[cid >> 4] * 128 + idxl[16 + (cid & 15u)]; }
;             const size_t o = ((size_t)u.pn * 16384 + (size_t)(u.pm * BM + row)) * 16;
;             typedef int i32x4 __attribute__((ext_vector_type(4)));
; #pragma unroll
;             for (int i = 0; i < 4; ++i) {
;     ...
;                 *(i32x4*)(eidx + o + 4 * i) = (i32x4){RT_PK(4 * i), RT_PK(4 * i + 1), RT_PK(4 * i + 2), RT_PK(4 * i + 3)};
	v_add_u32_e32 v0, v16, v0
	v_lshl_add_u32 v1, v1, 2, v16
	v_add_u32_e32 v2, v16, v2
	v_lshl_add_u32 v3, v3, 2, v16
	v_and_b32_e32 v4, 60, v4
	v_lshl_add_u32 v5, v5, 2, v16
	v_add_u32_e32 v6, v16, v6
	v_lshl_add_u32 v7, v7, 2, v16
	v_add_u32_e32 v4, v16, v4
	ds_read_b32 v0, v0
	ds_read_b32 v1, v1 offset:64
	ds_read_b32 v2, v2
	ds_read_b32 v3, v3 offset:64
	ds_read_b32 v10, v4
	ds_read_b32 v5, v5 offset:64
	ds_read_b32 v6, v6
	ds_read_b32 v7, v7 offset:64
	s_waitcnt lgkmcnt(0)
	v_lshl_add_u32 v0, v0, 7, v1
	v_ashrrev_i32_e32 v1, 31, v0
	v_lshl_add_u32 v4, v2, 7, v3
	v_lshlrev_b64 v[14:15], 3, v[0:1]
	v_lshl_add_u32 v10, v10, 7, v5
	v_lshl_add_u32 v12, v6, 7, v7
	v_lshl_add_u64 v[2:3], s[8:9], 0, v[14:15]
	v_ashrrev_i32_e32 v5, 31, v4
	v_max_f32_e32 v32, v13, v8
	v_min_f32_e32 v8, v13, v8
	global_load_dwordx2 v[170:171], v[2:3], off
	v_lshlrev_b64 v[18:19], 3, v[4:5]
	v_ashrrev_i32_e32 v11, 31, v10
	v_ashrrev_i32_e32 v13, 31, v12
	v_lshl_add_u64 v[2:3], s[8:9], 0, v[18:19]
	v_lshlrev_b64 v[20:21], 3, v[10:11]
	v_lshlrev_b64 v[22:23], 3, v[12:13]
	v_lshl_add_u64 v[6:7], s[8:9], 0, v[20:21]
	global_load_dwordx2 v[172:173], v[2:3], off
	global_load_dwordx2 v[174:175], v[6:7], off
	v_lshl_add_u64 v[2:3], s[8:9], 0, v[22:23]
	global_load_dwordx2 v[176:177], v[2:3], off
	v_min_f32_e32 v2, v9, v27
	v_min_f32_e32 v6, v25, v29
	v_max_f32_e32 v43, v2, v6
	v_min_f32_e32 v44, v2, v6
	v_and_b32_e32 v2, 0xffffff00, v34
	v_and_b32_e32 v51, 0xffffff00, v33
	v_max_f32_e32 v37, v9, v27
	v_max_f32_e32 v3, v25, v29
	v_sub_f32_e32 v2, v2, v51
	v_min_f32_e32 v9, v24, v28
	v_min_f32_e32 v25, v26, v30
	v_max_f32_e32 v41, v37, v3
	v_min_f32_e32 v42, v37, v3
	v_and_b32_e32 v3, 0xffffff00, v35
	v_mul_f32_e32 v2, 0x3fb8aa3b, v2
	v_max_f32_e32 v47, v9, v25
	v_min_f32_e32 v48, v9, v25
	v_exp_f32_e32 v25, v2
	v_sub_f32_e32 v2, v3, v51
	v_and_b32_e32 v6, 0xffffff00, v36
	v_mul_f32_e32 v2, 0x3fb8aa3b, v2
	v_max_f32_e32 v7, v24, v28
	v_max_f32_e32 v24, v26, v30
	v_max_f32_e32 v38, v17, v32
	v_exp_f32_e32 v26, v2
	v_sub_f32_e32 v2, v6, v51
	v_max_f32_e32 v45, v7, v24
	v_min_f32_e32 v46, v7, v24
	v_and_b32_e32 v7, 0xffffff00, v38
	v_mul_f32_e32 v2, 0x3fb8aa3b, v2
	v_min_f32_e32 v17, v17, v32
	v_exp_f32_e32 v27, v2
	v_sub_f32_e32 v2, v7, v51
	v_max_f32_e32 v39, v31, v8
	v_min_f32_e32 v40, v31, v8
	v_and_b32_e32 v8, 0xffffff00, v17
	v_mul_f32_e32 v2, 0x3fb8aa3b, v2
	v_exp_f32_e32 v28, v2
	v_sub_f32_e32 v2, v8, v51
	v_and_b32_e32 v9, 0xffffff00, v39
	v_mul_f32_e32 v2, 0x3fb8aa3b, v2
	v_exp_f32_e32 v29, v2
	v_sub_f32_e32 v2, v9, v51
	v_and_b32_e32 v31, 0xffffff00, v40
	v_mul_f32_e32 v2, 0x3fb8aa3b, v2
	v_exp_f32_e32 v30, v2
	v_sub_f32_e32 v2, v31, v51
	v_and_b32_e32 v32, 0xffffff00, v41
	v_mul_f32_e32 v2, 0x3fb8aa3b, v2
	v_exp_f32_e32 v31, v2
	v_sub_f32_e32 v2, v32, v51
	v_and_b32_e32 v34, 0xffffff00, v42
	v_mul_f32_e32 v2, 0x3fb8aa3b, v2
	v_exp_f32_e32 v6, v2
	v_sub_f32_e32 v2, v34, v51
	v_and_b32_e32 v35, 0xffffff00, v43
	v_mul_f32_e32 v2, 0x3fb8aa3b, v2
	v_exp_f32_e32 v7, v2
	v_sub_f32_e32 v2, v35, v51
	v_mul_f32_e32 v2, 0x3fb8aa3b, v2
	v_exp_f32_e32 v8, v2
	v_lshl_or_b32 v2, s18, 8, v128
	v_ashrrev_i32_e32 v3, 31, v2
	s_lshl_b64 s[4:5], s[16:17], 18
	v_lshl_add_u64 v[32:33], v[2:3], 4, s[4:5]
	s_mov_b32 s4, 0x7fc000
	v_sub_f32_e32 v24, v51, v51
	v_mul_f32_e32 v24, 0x3fb8aa3b, v24
	v_exp_f32_e32 v24, v24
	s_waitcnt vmcnt(0)
	v_lshrrev_b32_e32 v1, 9, v170
	v_and_or_b32 v2, v1, s4, v0
	v_and_b32_e32 v36, 0xffffff00, v44
	v_and_b32_e32 v37, 0xffffff00, v45
	v_and_b32_e32 v49, 0xffffff00, v46
	v_and_b32_e32 v50, 0xffffff00, v47
	v_and_b32_e32 v52, 0xffffff00, v48
	v_lshrrev_b32_e32 v0, 9, v172
	v_and_or_b32 v3, v0, s4, v4
	v_lshrrev_b32_e32 v0, 9, v174
	v_and_or_b32 v4, v0, s4, v10
	v_lshrrev_b32_e32 v0, 9, v176
	v_and_or_b32 v5, v0, s4, v12
	v_lshlrev_b64 v[12:13], 2, v[32:33]
	v_lshl_add_u64 v[0:1], s[12:13], 0, v[12:13]
	s_nop 0
	v_readfirstlane_b32 s98, v0
	v_readfirstlane_b32 s99, v1
	v_lshrrev_b32_e32 v202, 6, v128
	v_and_b32_e32 v203, 63, v128
	v_lshlrev_b32_e32 v202, 13, v202
	v_lshl_or_b32 v204, v203, 6, v202
	v_lshl_or_b32 v205, v203, 4, v202
	v_lshlrev_b32_e32 v203, 4, v203
	ds_write_b128 v204, v[2:5]
	v_lshrrev_b32_e32 v32, 2, v40
	v_add_f32_e32 v10, 0, v24
	v_add_f32_e32 v10, v25, v10
	v_add_f32_e32 v10, v26, v10
	v_add_f32_e32 v10, v27, v10
	v_sub_f32_e32 v2, v36, v51
	v_add_f32_e32 v10, v28, v10
	v_mul_f32_e32 v2, 0x3fb8aa3b, v2
	v_add_f32_e32 v10, v29, v10
	v_exp_f32_e32 v9, v2
	v_sub_f32_e32 v2, v37, v51
	v_add_f32_e32 v10, v30, v10
	v_mul_f32_e32 v2, 0x3fb8aa3b, v2
	v_sub_f32_e32 v3, v49, v51
	v_add_f32_e32 v10, v31, v10
	v_exp_f32_e32 v2, v2
	v_mul_f32_e32 v3, 0x3fb8aa3b, v3
	v_sub_f32_e32 v4, v50, v51
	v_add_f32_e32 v10, v6, v10
	v_exp_f32_e32 v3, v3
	v_mul_f32_e32 v4, 0x3fb8aa3b, v4
	v_sub_f32_e32 v5, v52, v51
	v_add_f32_e32 v10, v7, v10
	v_exp_f32_e32 v4, v4
	v_mul_f32_e32 v5, 0x3fb8aa3b, v5
	v_add_f32_e32 v10, v8, v10
	v_exp_f32_e32 v5, v5
	v_add_f32_e32 v10, v9, v10
	v_add_f32_e32 v10, v2, v10
	v_lshrrev_b32_e32 v11, 2, v38
	v_lshrrev_b32_e32 v15, 2, v17
	v_add_f32_e32 v10, v3, v10
	v_and_b32_e32 v11, 60, v11
	v_and_b32_e32 v14, 15, v38
	v_and_b32_e32 v15, 60, v15
	v_and_b32_e32 v17, 15, v17
	v_lshrrev_b32_e32 v22, 2, v39
	v_and_b32_e32 v23, 15, v39
	v_and_b32_e32 v33, 15, v40
	v_add_f32_e32 v10, v4, v10
	v_add_u32_e32 v11, v16, v11
	v_lshl_add_u32 v14, v14, 2, v16
	v_add_u32_e32 v15, v16, v15
	v_lshl_add_u32 v17, v17, 2, v16
	v_and_b32_e32 v22, 60, v22
	v_lshl_add_u32 v23, v23, 2, v16
	v_and_b32_e32 v32, 60, v32
	v_lshl_add_u32 v33, v33, 2, v16
	v_add_f32_e32 v10, v5, v10
	v_add_u32_e32 v22, v16, v22
	v_add_u32_e32 v32, v16, v32
	ds_read_b32 v11, v11
	ds_read_b32 v14, v14 offset:64
	ds_read_b32 v15, v15
	ds_read_b32 v17, v17 offset:64
	ds_read_b32 v34, v22
	ds_read_b32 v23, v23 offset:64
	ds_read_b32 v35, v32
	ds_read_b32 v33, v33 offset:64
	s_waitcnt lgkmcnt(6)
; #define RT_PK(q_) (ex[q_] | (int)((__float_as_uint(usc[ex[q_]]) >> 23) << 14))
;     __device__ __forceinline__ void fused(f32x4 (&acc)[2][2][4][2], const Unit& u, int wr, int wc, int fr, int fq, PG8_LAS unsigned char* lds, int wid, int lane) const {
;     ...
;             const float rs = 1.0f / sum;
;             asm volatile("s_waitcnt lgkmcnt(0)" ::: "memory");
;             int ex[16];
; #pragma unroll
;             for (int q = 0; q < 16; ++q) { const unsigned cid = __float_as_uint(best[q]) & 255u; ex[q] = idxl[cid >> 4] * 128 + idxl[16 + (cid & 15u)]; }
;             const size_t o = ((size_t)u.pn * 16384 + (size_t)(u.pm * BM + row)) * 16;
;             typedef int i32x4 __attribute__((ext_vector_type(4)));
; #pragma unroll
;             for (int i = 0; i < 4; ++i) {
;     ...
;                 *(i32x4*)(eidx + o + 4 * i) = (i32x4){RT_PK(4 * i), RT_PK(4 * i + 1), RT_PK(4 * i + 2), RT_PK(4 * i + 3)};
;                 *(f32x4*)(egate + o + 4 * i) = (f32x4){sc[4 * i] * rs * vsc[ex[4 * i]], sc[4 * i + 1] * rs * vsc[ex[4 * i + 1]], sc[4 * i + 2] * rs * vsc[ex[4 * i + 2]], sc[4 * i + 3] * rs * vsc[ex[4 * i + 3]]};
	v_lshl_add_u32 v14, v11, 7, v14
	v_div_scale_f32 v11, s[16:17], v10, v10, 1.0
	v_rcp_f32_e32 v36, v11
	s_waitcnt lgkmcnt(4)
	v_lshl_add_u32 v22, v15, 7, v17
	s_waitcnt lgkmcnt(2)
	v_lshl_add_u32 v32, v34, 7, v23
	s_waitcnt lgkmcnt(0)
	v_lshl_add_u32 v34, v35, 7, v33
	v_fma_f32 v15, -v11, v36, 1.0
	v_fmac_f32_e32 v36, v15, v36
	v_div_scale_f32 v15, vcc, 1.0, v10, 1.0
	v_mul_f32_e32 v17, v15, v36
	v_fma_f32 v23, -v11, v17, v15
	v_fmac_f32_e32 v17, v23, v36
	v_fma_f32 v11, -v11, v17, v15
	v_div_fmas_f32 v11, v11, v36, v17
	v_div_fixup_f32 v10, v11, v10, 1.0
	v_pk_mul_f32 v[24:25], v[24:25], v[10:11] op_sel_hi:[1,0]
	v_pk_mul_f32 v[26:27], v[26:27], v[10:11] op_sel_hi:[1,0]
	v_ashrrev_i32_e32 v15, 31, v14
	v_ashrrev_i32_e32 v33, 31, v32
	v_lshl_add_u64 v[12:13], s[10:11], 0, v[12:13]
	s_nop 0
	v_readfirstlane_b32 s100, v12
	v_readfirstlane_b32 s101, v13
	v_ashrrev_i32_e32 v23, 31, v22
	v_lshlrev_b64 v[36:37], 3, v[32:33]
	v_lshl_add_u64 v[38:39], s[8:9], 0, v[36:37]
	v_ashrrev_i32_e32 v35, 31, v34
	v_mul_f32_e32 v18, v24, v171
	v_mul_f32_e32 v19, v25, v173
	v_lshlrev_b64 v[24:25], 3, v[14:15]
	v_mul_f32_e32 v20, v26, v175
	v_mul_f32_e32 v21, v27, v177
	ds_write_b128 v204, v[18:21] offset:4096
	v_lshlrev_b64 v[26:27], 3, v[22:23]
	s_nop 0
	v_lshl_add_u64 v[18:19], s[8:9], 0, v[24:25]
	v_lshl_add_u64 v[20:21], s[8:9], 0, v[26:27]
	global_load_dwordx2 v[178:179], v[18:19], off
	global_load_dwordx2 v[180:181], v[20:21], off
	global_load_dwordx2 v[182:183], v[38:39], off
	v_lshlrev_b64 v[38:39], 3, v[34:35]
	v_lshl_add_u64 v[18:19], s[8:9], 0, v[38:39]
	global_load_dwordx2 v[184:185], v[18:19], off
	s_waitcnt vmcnt(3)
	v_lshrrev_b32_e32 v11, 9, v178
	v_and_or_b32 v18, v11, s4, v14
	s_waitcnt vmcnt(2)
	v_lshrrev_b32_e32 v11, 9, v180
	v_and_or_b32 v19, v11, s4, v22
	s_waitcnt vmcnt(1)
	v_lshrrev_b32_e32 v11, 9, v182
	v_and_or_b32 v20, v11, s4, v32
	s_waitcnt vmcnt(0)
	v_lshrrev_b32_e32 v11, 9, v184
	v_and_or_b32 v21, v11, s4, v34
	ds_write_b128 v204, v[18:21] offset:16
	v_lshrrev_b32_e32 v11, 2, v41
	v_lshrrev_b32_e32 v15, 2, v42
	v_lshrrev_b32_e32 v18, 2, v43
	v_lshrrev_b32_e32 v20, 2, v44
	v_and_b32_e32 v11, 60, v11
	v_and_b32_e32 v14, 15, v41
	v_and_b32_e32 v15, 60, v15
	v_and_b32_e32 v17, 15, v42
	v_and_b32_e32 v18, 60, v18
	v_and_b32_e32 v19, 15, v43
	v_and_b32_e32 v20, 60, v20
	v_and_b32_e32 v21, 15, v44
	v_add_u32_e32 v11, v16, v11
	v_lshl_add_u32 v14, v14, 2, v16
	v_add_u32_e32 v15, v16, v15
	v_lshl_add_u32 v17, v17, 2, v16
	v_add_u32_e32 v18, v16, v18
	v_lshl_add_u32 v19, v19, 2, v16
	v_add_u32_e32 v20, v16, v20
	v_lshl_add_u32 v21, v21, 2, v16
	ds_read_b32 v11, v11
	ds_read_b32 v14, v14 offset:64
	ds_read_b32 v15, v15
	ds_read_b32 v17, v17 offset:64
	ds_read_b32 v18, v18
	ds_read_b32 v19, v19 offset:64
	ds_read_b32 v20, v20
	ds_read_b32 v21, v21 offset:64
	s_waitcnt lgkmcnt(6)
	v_lshl_add_u32 v14, v11, 7, v14
	s_waitcnt lgkmcnt(4)
	v_lshl_add_u32 v22, v15, 7, v17
	s_waitcnt lgkmcnt(2)
	v_lshl_add_u32 v32, v18, 7, v19
	v_pk_mul_f32 v[18:19], v[28:29], v[10:11] op_sel_hi:[1,0]
	s_waitcnt lgkmcnt(0)
	v_lshl_add_u32 v34, v20, 7, v21
	v_pk_mul_f32 v[20:21], v[30:31], v[10:11] op_sel_hi:[1,0]
	v_ashrrev_i32_e32 v15, 31, v14
	v_ashrrev_i32_e32 v33, 31, v32
	v_ashrrev_i32_e32 v23, 31, v22
	v_lshlrev_b64 v[28:29], 3, v[32:33]
	v_lshl_add_u64 v[30:31], s[8:9], 0, v[28:29]
	v_ashrrev_i32_e32 v35, 31, v34
	v_mul_f32_e32 v20, v20, v183
	v_mul_f32_e32 v21, v21, v185
	v_mul_f32_e32 v18, v18, v179
	v_mul_f32_e32 v19, v19, v181
	v_lshlrev_b64 v[24:25], 3, v[14:15]
	ds_write_b128 v204, v[18:21] offset:4112
	v_lshlrev_b64 v[26:27], 3, v[22:23]
	s_nop 0
	v_lshl_add_u64 v[18:19], s[8:9], 0, v[24:25]
	v_lshl_add_u64 v[20:21], s[8:9], 0, v[26:27]
	global_load_dwordx2 v[186:187], v[18:19], off
	global_load_dwordx2 v[188:189], v[20:21], off
	global_load_dwordx2 v[190:191], v[30:31], off
	v_lshlrev_b64 v[30:31], 3, v[34:35]
	v_lshl_add_u64 v[18:19], s[8:9], 0, v[30:31]
	global_load_dwordx2 v[192:193], v[18:19], off
	s_waitcnt vmcnt(3)
; #define RT_PK(q_) (ex[q_] | (int)((__float_as_uint(usc[ex[q_]]) >> 23) << 14))
;     __device__ __forceinline__ void fused(f32x4 (&acc)[2][2][4][2], const Unit& u, int wr, int wc, int fr, int fq, PG8_LAS unsigned char* lds, int wid, int lane) const {
;     ...
;             for (int q = 0; q < 16; ++q) { const unsigned cid = __float_as_uint(best[q]) & 255u; ex[q] = idxl[cid >> 4] * 128 + idxl[16 + (cid & 15u)]; }
;             const size_t o = ((size_t)u.pn * 16384 + (size_t)(u.pm * BM + row)) * 16;
;             typedef int i32x4 __attribute__((ext_vector_type(4)));
; #pragma unroll
;             for (int i = 0; i < 4; ++i) {
;     ...
;                 *(i32x4*)(eidx + o + 4 * i) = (i32x4){RT_PK(4 * i), RT_PK(4 * i + 1), RT_PK(4 * i + 2), RT_PK(4 * i + 3)};
;                 *(f32x4*)(egate + o + 4 * i) = (f32x4){sc[4 * i] * rs * vsc[ex[4 * i]], sc[4 * i + 1] * rs * vsc[ex[4 * i + 1]], sc[4 * i + 2] * rs * vsc[ex[4 * i + 2]], sc[4 * i + 3] * rs * vsc[ex[4 * i + 3]]};
	v_lshrrev_b32_e32 v11, 9, v186
	v_and_or_b32 v18, v11, s4, v14
	s_waitcnt vmcnt(2)
	v_lshrrev_b32_e32 v11, 9, v188
	v_and_or_b32 v19, v11, s4, v22
	s_waitcnt vmcnt(1)
	v_lshrrev_b32_e32 v11, 9, v190
	v_and_or_b32 v20, v11, s4, v32
	s_waitcnt vmcnt(0)
	v_lshrrev_b32_e32 v11, 9, v192
	v_and_or_b32 v21, v11, s4, v34
	ds_write_b128 v204, v[18:21] offset:32
	v_lshrrev_b32_e32 v11, 2, v45
	v_lshrrev_b32_e32 v15, 2, v46
	v_lshrrev_b32_e32 v18, 2, v47
	v_lshrrev_b32_e32 v20, 2, v48
	v_and_b32_e32 v11, 60, v11
	v_and_b32_e32 v14, 15, v45
	v_and_b32_e32 v15, 60, v15
	v_and_b32_e32 v17, 15, v46
	v_and_b32_e32 v18, 60, v18
	v_and_b32_e32 v19, 15, v47
	v_and_b32_e32 v20, 60, v20
	v_add_u32_e32 v11, v16, v11
	v_lshl_add_u32 v14, v14, 2, v16
	v_add_u32_e32 v15, v16, v15
	v_lshl_add_u32 v17, v17, 2, v16
	v_add_u32_e32 v18, v16, v18
	v_lshl_add_u32 v19, v19, 2, v16
	v_add_u32_e32 v20, v16, v20
	v_and_b32_e32 v21, 15, v48
	v_lshl_add_u32 v16, v21, 2, v16
	ds_read_b32 v11, v11
	ds_read_b32 v14, v14 offset:64
	ds_read_b32 v15, v15
	ds_read_b32 v17, v17 offset:64
	ds_read_b32 v18, v18
	ds_read_b32 v19, v19 offset:64
	ds_read_b32 v20, v20
	ds_read_b32 v21, v16 offset:64
	s_waitcnt lgkmcnt(6)
	v_lshl_add_u32 v14, v11, 7, v14
	s_waitcnt lgkmcnt(4)
	v_lshl_add_u32 v16, v15, 7, v17
	s_waitcnt lgkmcnt(2)
	v_lshl_add_u32 v18, v18, 7, v19
	v_pk_mul_f32 v[6:7], v[6:7], v[10:11] op_sel_hi:[1,0]
	v_pk_mul_f32 v[8:9], v[8:9], v[10:11] op_sel_hi:[1,0]
	v_ashrrev_i32_e32 v15, 31, v14
	v_ashrrev_i32_e32 v19, 31, v18
	s_waitcnt lgkmcnt(0)
	v_lshl_add_u32 v20, v20, 7, v21
	v_lshlrev_b64 v[22:23], 3, v[14:15]
	v_ashrrev_i32_e32 v17, 31, v16
	v_ashrrev_i32_e32 v21, 31, v20
	v_mul_f32_e32 v8, v8, v191
	v_mul_f32_e32 v9, v9, v193
	v_mul_f32_e32 v6, v6, v187
	v_mul_f32_e32 v7, v7, v189
	v_lshlrev_b64 v[26:27], 3, v[18:19]
	ds_write_b128 v204, v[6:9] offset:4128
	v_lshlrev_b64 v[24:25], 3, v[16:17]
	v_lshl_add_u64 v[28:29], s[8:9], 0, v[26:27]
	v_lshl_add_u64 v[6:7], s[8:9], 0, v[22:23]
	v_lshl_add_u64 v[8:9], s[8:9], 0, v[24:25]
	global_load_dwordx2 v[194:195], v[6:7], off
	global_load_dwordx2 v[196:197], v[8:9], off
	global_load_dwordx2 v[198:199], v[28:29], off
	v_lshlrev_b64 v[28:29], 3, v[20:21]
	v_lshl_add_u64 v[6:7], s[8:9], 0, v[28:29]
	global_load_dwordx2 v[200:201], v[6:7], off
	s_waitcnt vmcnt(3)
	v_lshrrev_b32_e32 v6, 9, v194
	s_waitcnt vmcnt(2)
	v_lshrrev_b32_e32 v7, 9, v196
	s_waitcnt vmcnt(1)
	v_lshrrev_b32_e32 v8, 9, v198
	v_and_or_b32 v6, v6, s4, v14
	v_and_or_b32 v7, v7, s4, v16
	s_waitcnt vmcnt(0)
	v_lshrrev_b32_e32 v9, 9, v200
	v_and_or_b32 v8, v8, s4, v18
	v_and_or_b32 v9, v9, s4, v20
	ds_write_b128 v204, v[6:9] offset:48
	v_pk_mul_f32 v[0:1], v[2:3], v[10:11] op_sel_hi:[1,0]
	v_pk_mul_f32 v[2:3], v[4:5], v[10:11] op_sel_hi:[1,0]
	v_mul_f32_e32 v0, v0, v195
	v_mul_f32_e32 v1, v1, v197
	v_mul_f32_e32 v2, v2, v199
	v_mul_f32_e32 v3, v3, v201
	ds_write_b128 v204, v[0:3] offset:4144
	s_waitcnt lgkmcnt(0)
	ds_read_b128 v[140:143], v205
	ds_read_b128 v[144:147], v205 offset:1024
	ds_read_b128 v[148:151], v205 offset:2048
	ds_read_b128 v[152:155], v205 offset:3072
	ds_read_b128 v[156:159], v205 offset:4096
	ds_read_b128 v[160:163], v205 offset:5120
	ds_read_b128 v[164:167], v205 offset:6144
	ds_read_b128 v[206:209], v205 offset:7168
	s_waitcnt lgkmcnt(0)
	global_store_dwordx4 v203, v[140:143], s[98:99] sc0 sc1
	global_store_dwordx4 v203, v[144:147], s[98:99] offset:1024 sc0 sc1
	global_store_dwordx4 v203, v[148:151], s[98:99] offset:2048 sc0 sc1
	global_store_dwordx4 v203, v[152:155], s[98:99] offset:3072 sc0 sc1
	global_store_dwordx4 v203, v[156:159], s[100:101] sc0 sc1
	global_store_dwordx4 v203, v[160:163], s[100:101] offset:1024 sc0 sc1
	global_store_dwordx4 v203, v[164:167], s[100:101] offset:2048 sc0 sc1
	global_store_dwordx4 v203, v[206:209], s[100:101] offset:3072 sc0 sc1

; #define PG8_LAS __attribute__((address_space(3)))
;     __device__ __forceinline__ void fused(f32x4 (&acc)[2][2][4][2], const Unit& u, int wr, int wc, int fr, int fq, PG8_LAS unsigned char* lds, int wid, int lane) const {
;     ...
;         if (half == 0) {
;             PG8_LAS int* idxl = (PG8_LAS int*)(lds + 65536) + row * 32;
;             float v0[16], v1[16];
; #pragma unroll
;             for (int q = 0; q < 16; ++q) { const unsigned b0 = __float_as_uint(top0[q]), b1 = __float_as_uint(top1[q]);
;                 v0[q] = __uint_as_float(b0 & ~127u); v1[q] = __uint_as_float(b1 & ~127u); idxl[q] = (int)(b0 & 127u); idxl[16 + q] = (int)(b1 & 127u); }
;             float best[16];
;             { float cv[16]; cv[0] = __uint_as_float((__float_as_uint(v0[0] + v1[0]) & ~255u) | 0u); cv[1] = __uint_as_float((__float_as_uint(v0[0] + v1[1]) & ~255u) | 1u); cv[2] = __uint_as_float((__float_as_uint(v0[0] + v1[2]) & ~255u) | 2u); cv[3] = __uint_as_float((__float_as_uint(v0[0] + v1[3]) & ~255u) | 3u); cv[4] = __uint_as_float((__float_as_uint(v0[0] + v1[4]) & ~255u) | 4u); cv[5] = __uint_as_float((__float_as_uint(v0[0] + v1[5]) & ~255u) | 5u); cv[6] = __uint_as_float((__float_as_uint(v0[0] + v1[6]) & ~255u) | 6u); cv[7] = __uint_as_float((__float_as_uint(v0[0] + v1[7]) & ~255u) | 7u); cv[8] = __uint_as_float((__float_as_uint(v0[0] + v1[8]) & ~255u) | 8u); cv[9] = __uint_as_float((__float_as_uint(v0[0] + v1[9]) & ~255u) | 9u); cv[10] = __uint_as_float((__float_as_uint(v0[0] + v1[10]) & ~255u) | 10u); cv[11] = __uint_as_float((__float_as_uint(v0[0] + v1[11]) & ~255u) | 11u); cv[12] = __uint_as_float((__float_as_uint(v0[0] + v1[12]) & ~255u) | 12u); cv[13] = __uint_as_float((__float_as_uint(v0[0] + v1[13]) & ~255u) | 13u); cv[14] = __uint_as_float((__float_as_uint(v0[0] + v1[14]) & ~255u) | 14u); cv[15] = __uint_as_float((__float_as_uint(v0[0] + v1[15]) & ~255u) | 15u); sort16_desc(cv);
; #pragma unroll
;               for (int q = 0; q < 16; ++q) best[q] = cv[q]; }
.LBB0_606:
	s_waitcnt lgkmcnt(0)
	s_barrier
	s_and_b64 vcc, exec, s[4:5]
	s_cbranch_vccnz .LBB0_608
	v_lshl_add_u32 v16, v128, 7, 0
	v_add_u32_e32 v16, 0x10000, v16
	v_and_b32_e32 v17, 0xffffff80, v12
	v_and_b32_e32 v18, 0xffffff80, v13
	v_and_b32_e32 v21, 0x7f, v77
	v_and_b32_e32 v20, 0x7f, v76
	v_and_b32_e32 v13, 0x7f, v13
	v_and_b32_e32 v12, 0x7f, v12
	v_and_b32_e32 v26, 0xffffff80, v14
	v_and_b32_e32 v28, 0xffffff80, v15
	v_and_b32_e32 v23, 0x7f, v79
	v_and_b32_e32 v22, 0x7f, v78
	v_and_b32_e32 v15, 0x7f, v15
	v_and_b32_e32 v14, 0x7f, v14
	ds_write_b128 v16, v[20:23]
	ds_write_b128 v16, v[12:15] offset:64
	v_and_b32_e32 v21, 0xffffff80, v8
	v_and_b32_e32 v23, 0xffffff80, v9
	v_and_b32_e32 v13, 0x7f, v73
	v_and_b32_e32 v12, 0x7f, v72
	v_and_b32_e32 v9, 0x7f, v9
	v_and_b32_e32 v8, 0x7f, v8
	v_and_b32_e32 v30, 0xffffff80, v10
	v_and_b32_e32 v32, 0xffffff80, v11
	v_and_b32_e32 v15, 0x7f, v75
	v_and_b32_e32 v14, 0x7f, v74
	v_and_b32_e32 v11, 0x7f, v11
	v_and_b32_e32 v10, 0x7f, v10
	v_and_b32_e32 v19, 0xffffff80, v76
	ds_write_b128 v16, v[12:15] offset:16
	ds_write_b128 v16, v[8:11] offset:80
	v_and_b32_e32 v13, 0xffffff80, v4
	v_and_b32_e32 v15, 0xffffff80, v5
	v_and_b32_e32 v9, 0x7f, v69
	v_and_b32_e32 v8, 0x7f, v68
	v_and_b32_e32 v5, 0x7f, v5
	v_and_b32_e32 v4, 0x7f, v4
	v_and_b32_e32 v34, 0xffffff80, v6
	v_and_b32_e32 v36, 0xffffff80, v7
	v_and_b32_e32 v11, 0x7f, v71
	v_and_b32_e32 v10, 0x7f, v70
	v_and_b32_e32 v7, 0x7f, v7
	v_and_b32_e32 v6, 0x7f, v6
	ds_write_b128 v16, v[8:11] offset:32
	ds_write_b128 v16, v[4:7] offset:96
	v_and_b32_e32 v5, 0x7f, v65
	v_and_b32_e32 v4, 0x7f, v64
	v_and_b32_e32 v41, 0xffffff80, v2
	v_and_b32_e32 v42, 0xffffff80, v3
	v_and_b32_e32 v7, 0x7f, v67
	v_and_b32_e32 v6, 0x7f, v66
	v_and_b32_e32 v11, 0x7f, v3
	v_and_b32_e32 v10, 0x7f, v2
	v_add_f32_e32 v2, v19, v17
	s_movk_i32 s3, 0xff00
	v_add_f32_e32 v3, v19, v18
	v_and_b32_e32 v24, 0xffffff80, v77
	ds_write_b128 v16, v[4:7] offset:48
	v_and_b32_e32 v2, 0xffffff00, v2
	v_and_or_b32 v3, v3, s3, 1
	v_add_f32_e32 v4, v19, v26
	v_add_f32_e32 v5, v19, v28
	v_and_b32_e32 v40, 0xffffff80, v1
	v_and_b32_e32 v9, 0x7f, v1
	v_and_b32_e32 v8, 0x7f, v0
	v_and_or_b32 v4, v4, s3, 2
	v_and_or_b32 v5, v5, s3, 3
	v_add_f32_e32 v48, v24, v17
	v_add_f32_e32 v49, v24, v18
	ds_write_b128 v16, v[8:11] offset:112
	v_add_f32_e32 v6, v19, v21
	v_add_f32_e32 v7, v19, v23
	v_add_f32_e32 v11, v19, v15
	v_add_f32_e32 v15, v19, v36
	v_add_f32_e32 v36, v19, v40
	v_max_f32_e32 v40, v2, v3
	v_min_f32_e32 v2, v2, v3
	v_max_f32_e32 v3, v5, v5
	v_and_or_b32 v48, v48, s3, 16
	v_and_or_b32 v49, v49, s3, 17
	v_add_f32_e32 v50, v24, v26
	v_add_f32_e32 v51, v24, v28
	v_and_or_b32 v6, v6, s3, 4
	v_and_or_b32 v7, v7, s3, 5
	v_add_f32_e32 v8, v19, v30
	v_add_f32_e32 v9, v19, v32
	v_max_f32_e32 v5, v4, v3
	v_min_f32_e32 v3, v4, v3
	v_and_or_b32 v50, v50, s3, 18
	v_and_or_b32 v51, v51, s3, 19
	v_and_or_b32 v8, v8, s3, 6
	v_and_or_b32 v9, v9, s3, 7
	v_max_f32_e32 v4, v40, v5
	v_min_f32_e32 v5, v40, v5
	v_max_f32_e32 v40, v2, v3
	v_add_f32_e32 v52, v24, v21
	v_add_f32_e32 v23, v24, v23
	v_add_f32_e32 v30, v24, v30
	v_add_f32_e32 v24, v24, v32
	v_max_f32_e32 v58, v48, v49
	v_min_f32_e32 v48, v48, v49
	v_max_f32_e32 v49, v51, v51
	v_min_f32_e32 v2, v2, v3
	v_max_f32_e32 v3, v40, v5
	v_min_f32_e32 v5, v40, v5
	v_max_f32_e32 v40, v6, v7
	v_min_f32_e32 v6, v6, v7
	v_max_f32_e32 v7, v9, v9
	v_and_or_b32 v52, v52, s3, 20
	v_and_or_b32 v23, v23, s3, 21
	v_and_or_b32 v30, v30, s3, 22
	v_and_or_b32 v24, v24, s3, 23
	v_max_f32_e32 v51, v50, v49
	v_min_f32_e32 v49, v50, v49
	v_max_f32_e32 v9, v8, v7
	v_min_f32_e32 v7, v8, v7
	v_max_f32_e32 v50, v58, v51
	v_min_f32_e32 v51, v58, v51
	v_max_f32_e32 v58, v48, v49
	v_max_f32_e32 v8, v40, v9
	v_min_f32_e32 v9, v40, v9
	v_max_f32_e32 v40, v6, v7
	v_min_f32_e32 v48, v48, v49
	v_max_f32_e32 v49, v58, v51
	v_min_f32_e32 v51, v58, v51
	v_max_f32_e32 v58, v52, v23
	v_min_f32_e32 v23, v52, v23
	v_max_f32_e32 v52, v30, v24
	v_min_f32_e32 v24, v30, v24
	v_min_f32_e32 v6, v6, v7
	v_max_f32_e32 v7, v40, v9
	v_min_f32_e32 v9, v40, v9
	v_max_f32_e32 v30, v58, v52
	v_min_f32_e32 v52, v58, v52
	v_max_f32_e32 v58, v23, v24
	v_max_f32_e32 v40, v4, v8
	v_min_f32_e32 v4, v4, v8
	v_max_f32_e32 v8, v5, v9
	v_min_f32_e32 v23, v23, v24
	v_max_f32_e32 v24, v58, v52
	v_min_f32_e32 v52, v58, v52
	v_and_b32_e32 v25, 0xffffff80, v78
	v_add_f32_e32 v10, v19, v13
	v_min_f32_e32 v5, v5, v9
	v_max_f32_e32 v9, v8, v4
	v_min_f32_e32 v4, v8, v4
	v_max_f32_e32 v8, v3, v7
	v_min_f32_e32 v3, v3, v7
	v_max_f32_e32 v7, v2, v6
	v_max_f32_e32 v58, v50, v30
	v_min_f32_e32 v30, v50, v30
	v_max_f32_e32 v50, v51, v52
	v_and_or_b32 v10, v10, s3, 8
	v_and_or_b32 v11, v11, s3, 9
	v_add_f32_e32 v13, v19, v34
	v_min_f32_e32 v2, v2, v6
	v_max_f32_e32 v6, v7, v3
	v_min_f32_e32 v3, v7, v3
	v_add_f32_e32 v32, v25, v17
	v_add_f32_e32 v53, v25, v18
	v_min_f32_e32 v51, v51, v52
	v_max_f32_e32 v52, v50, v30
	v_min_f32_e32 v30, v50, v30
	v_max_f32_e32 v50, v49, v24
	v_min_f32_e32 v24, v49, v24
	v_max_f32_e32 v49, v48, v23
	v_and_or_b32 v13, v13, s3, 10
	v_and_or_b32 v15, v15, s3, 11
	v_max_f32_e32 v7, v8, v9
	v_min_f32_e32 v8, v8, v9
	v_max_f32_e32 v9, v6, v4
	v_min_f32_e32 v4, v6, v4
	v_max_f32_e32 v6, v3, v5
	v_min_f32_e32 v3, v3, v5
	v_max_f32_e32 v5, v11, v11
	v_and_or_b32 v32, v32, s3, 32
	v_and_or_b32 v53, v53, s3, 33
	v_add_f32_e32 v54, v25, v26
	v_add_f32_e32 v55, v25, v28
	v_min_f32_e32 v23, v48, v23
	v_max_f32_e32 v48, v49, v24
	v_min_f32_e32 v24, v49, v24
	v_and_b32_e32 v27, 0xffffff80, v79
	v_and_b32_e32 v38, 0xffffff80, v0
	v_max_f32_e32 v11, v10, v5
	v_min_f32_e32 v5, v10, v5
	v_max_f32_e32 v10, v15, v15
;     __device__ __forceinline__ void fused(f32x4 (&acc)[2][2][4][2], const Unit& u, int wr, int wc, int fr, int fq, PG8_LAS unsigned char* lds, int wid, int lane) const {
;     ...
;             { float cv[16]; cv[0] = __uint_as_float((__float_as_uint(v0[1] + v1[0]) & ~255u) | 16u); cv[1] = __uint_as_float((__float_as_uint(v0[1] + v1[1]) & ~255u) | 17u); cv[2] = __uint_as_float((__float_as_uint(v0[1] + v1[2]) & ~255u) | 18u); cv[3] = __uint_as_float((__float_as_uint(v0[1] + v1[3]) & ~255u) | 19u); cv[4] = __uint_as_float((__float_as_uint(v0[1] + v1[4]) & ~255u) | 20u); cv[5] = __uint_as_float((__float_as_uint(v0[1] + v1[5]) & ~255u) | 21u); cv[6] = __uint_as_float((__float_as_uint(v0[1] + v1[6]) & ~255u) | 22u); cv[7] = __uint_as_float((__float_as_uint(v0[1] + v1[7]) & ~255u) | 23u); cv[8] = __uint_as_float((__float_as_uint(v0[2] + v1[0]) & ~255u) | 32u); cv[9] = __uint_as_float((__float_as_uint(v0[2] + v1[1]) & ~255u) | 33u); cv[10] = __uint_as_float((__float_as_uint(v0[2] + v1[2]) & ~255u) | 34u); cv[11] = __uint_as_float((__float_as_uint(v0[2] + v1[3]) & ~255u) | 35u); cv[12] = __uint_as_float((__float_as_uint(v0[2] + v1[4]) & ~255u) | 36u); cv[13] = __uint_as_float((__float_as_uint(v0[3] + v1[0]) & ~255u) | 48u); cv[14] = __uint_as_float((__float_as_uint(v0[3] + v1[1]) & ~255u) | 49u); cv[15] = __uint_as_float((__float_as_uint(v0[3] + v1[2]) & ~255u) | 50u); sort16_desc(cv); merge_top16(best, cv); }
	v_and_or_b32 v54, v54, s3, 34
	v_and_or_b32 v55, v55, s3, 35
	v_max_f32_e32 v49, v50, v52
	v_min_f32_e32 v50, v50, v52
	v_max_f32_e32 v52, v48, v30
	v_min_f32_e32 v30, v48, v30
	v_max_f32_e32 v48, v24, v51
	v_min_f32_e32 v24, v24, v51
	v_max_f32_e32 v51, v53, v53
	v_add_f32_e32 v34, v19, v38
	v_max_f32_e32 v15, v13, v10
	v_min_f32_e32 v10, v13, v10
	v_add_f32_e32 v21, v25, v21
	v_add_f32_e32 v25, v27, v17
	v_max_f32_e32 v53, v32, v51
	v_min_f32_e32 v32, v32, v51
	v_max_f32_e32 v51, v55, v55
	v_and_or_b32 v34, v34, s3, 12
	v_and_or_b32 v36, v36, s3, 13
	v_add_f32_e32 v38, v19, v41
	v_add_f32_e32 v19, v19, v42
	v_max_f32_e32 v13, v11, v15
	v_min_f32_e32 v11, v11, v15
	v_max_f32_e32 v15, v5, v10
	v_and_or_b32 v21, v21, s3, 36
	v_and_or_b32 v25, v25, s3, 48
	v_add_f32_e32 v56, v27, v18
	v_add_f32_e32 v57, v27, v26
	v_max_f32_e32 v55, v54, v51
	v_min_f32_e32 v51, v54, v51
	v_and_or_b32 v38, v38, s3, 14
	v_and_or_b32 v19, v19, s3, 15
	v_min_f32_e32 v5, v5, v10
	v_max_f32_e32 v10, v15, v11
	v_min_f32_e32 v11, v15, v11
	v_max_f32_e32 v15, v36, v36
	v_and_or_b32 v56, v56, s3, 49
	v_and_or_b32 v57, v57, s3, 50
	v_max_f32_e32 v54, v53, v55
	v_min_f32_e32 v53, v53, v55
	v_max_f32_e32 v55, v32, v51
	v_max_f32_e32 v36, v34, v15
	v_min_f32_e32 v15, v34, v15
	v_max_f32_e32 v34, v38, v38
	v_min_f32_e32 v32, v32, v51
	v_max_f32_e32 v51, v55, v53
	v_min_f32_e32 v53, v55, v53
	v_max_f32_e32 v55, v21, v25
	v_min_f32_e32 v21, v21, v25
	v_max_f32_e32 v25, v57, v57
	v_max_f32_e32 v38, v34, v19
	v_min_f32_e32 v19, v34, v19
	v_max_f32_e32 v57, v56, v25
	v_min_f32_e32 v25, v56, v25
	v_max_f32_e32 v34, v36, v38
	v_min_f32_e32 v36, v36, v38
	v_max_f32_e32 v38, v15, v19
	v_max_f32_e32 v56, v55, v57
	v_min_f32_e32 v55, v55, v57
	v_max_f32_e32 v57, v21, v25
	v_min_f32_e32 v15, v15, v19
	v_max_f32_e32 v19, v38, v36
	v_min_f32_e32 v36, v38, v36
	v_min_f32_e32 v21, v21, v25
	v_max_f32_e32 v25, v57, v55
	v_min_f32_e32 v55, v57, v55
	v_max_f32_e32 v38, v13, v34
	v_min_f32_e32 v13, v13, v34
	v_max_f32_e32 v34, v11, v36
	v_max_f32_e32 v57, v54, v56
	v_min_f32_e32 v54, v54, v56
	v_max_f32_e32 v56, v53, v55
	v_min_f32_e32 v11, v11, v36
	v_max_f32_e32 v36, v34, v13
	v_min_f32_e32 v13, v34, v13
	v_max_f32_e32 v34, v10, v19
	v_min_f32_e32 v10, v10, v19
	v_max_f32_e32 v19, v5, v15
	v_min_f32_e32 v53, v53, v55
	v_max_f32_e32 v55, v56, v54
	v_min_f32_e32 v54, v56, v54
	v_max_f32_e32 v56, v51, v25
	v_min_f32_e32 v25, v51, v25
	v_max_f32_e32 v51, v32, v21
	v_min_f32_e32 v5, v5, v15
	v_max_f32_e32 v15, v19, v10
	v_min_f32_e32 v21, v32, v21
	v_max_f32_e32 v32, v51, v25
	v_min_f32_e32 v10, v19, v10
	v_max_f32_e32 v19, v34, v36
	v_min_f32_e32 v34, v34, v36
	v_max_f32_e32 v36, v15, v13
	v_min_f32_e32 v13, v15, v13
	v_min_f32_e32 v25, v51, v25
	v_max_f32_e32 v51, v56, v55
	v_min_f32_e32 v55, v56, v55
	v_max_f32_e32 v56, v32, v54
	v_min_f32_e32 v32, v32, v54
	v_max_f32_e32 v15, v10, v11
	v_min_f32_e32 v10, v10, v11
	v_min_f32_e32 v11, v40, v38
	v_max_f32_e32 v41, v4, v13
	v_max_f32_e32 v54, v25, v53
	v_min_f32_e32 v25, v25, v53
	v_min_f32_e32 v53, v58, v57
	v_max_f32_e32 v59, v30, v32
	v_min_f32_e32 v4, v4, v13
	v_max_f32_e32 v13, v41, v11
	v_min_f32_e32 v11, v41, v11
	v_max_f32_e32 v41, v8, v34
	v_min_f32_e32 v8, v8, v34
	v_max_f32_e32 v34, v3, v10
	v_min_f32_e32 v30, v30, v32
	v_max_f32_e32 v32, v59, v53
	v_min_f32_e32 v53, v59, v53
	v_max_f32_e32 v59, v50, v55
	v_min_f32_e32 v50, v50, v55
	v_max_f32_e32 v55, v24, v25
	v_min_f32_e32 v3, v3, v10
	v_max_f32_e32 v10, v34, v8
	v_min_f32_e32 v8, v34, v8
	v_min_f32_e32 v24, v24, v25
	v_max_f32_e32 v25, v55, v50
	v_min_f32_e32 v50, v55, v50
	v_max_f32_e32 v34, v41, v13
	v_min_f32_e32 v13, v41, v13
	v_max_f32_e32 v41, v10, v11
	v_min_f32_e32 v10, v10, v11
	v_max_f32_e32 v11, v8, v4
	v_min_f32_e32 v4, v8, v4
	v_max_f32_e32 v8, v7, v19
	v_min_f32_e32 v7, v7, v19
	v_max_f32_e32 v19, v6, v15
	v_max_f32_e32 v55, v59, v32
	v_min_f32_e32 v32, v59, v32
	v_max_f32_e32 v59, v25, v53
	v_min_f32_e32 v25, v25, v53
	v_max_f32_e32 v53, v50, v30
	v_min_f32_e32 v30, v50, v30
	v_max_f32_e32 v50, v49, v51
	v_min_f32_e32 v49, v49, v51
	v_max_f32_e32 v51, v48, v54
	v_min_f32_e32 v6, v6, v15
	v_max_f32_e32 v15, v19, v7
	v_min_f32_e32 v7, v19, v7
	v_max_f32_e32 v19, v9, v36
	v_min_f32_e32 v9, v9, v36
	v_max_f32_e32 v36, v2, v5
	v_min_f32_e32 v48, v48, v54
	v_max_f32_e32 v54, v51, v49
	v_min_f32_e32 v49, v51, v49
	v_max_f32_e32 v51, v52, v56
	v_min_f32_e32 v52, v52, v56
	v_max_f32_e32 v56, v23, v21
	v_min_f32_e32 v2, v2, v5
	v_max_f32_e32 v5, v36, v9
	v_min_f32_e32 v9, v36, v9
	v_max_f32_e32 v36, v19, v15
	v_min_f32_e32 v21, v23, v21
	v_max_f32_e32 v23, v56, v52
	v_min_f32_e32 v52, v56, v52
	v_and_b32_e32 v20, 0xffffff80, v72
	v_min_f32_e32 v15, v19, v15
	v_max_f32_e32 v19, v5, v7
	v_min_f32_e32 v5, v5, v7
	v_max_f32_e32 v7, v9, v6
	v_min_f32_e32 v6, v9, v6
	v_min_f32_e32 v9, v8, v34
	v_min_f32_e32 v42, v36, v13
	v_max_f32_e32 v56, v51, v54
	v_min_f32_e32 v51, v51, v54
	v_max_f32_e32 v54, v23, v49
	v_min_f32_e32 v23, v23, v49
	v_max_f32_e32 v49, v52, v48
	v_min_f32_e32 v48, v52, v48
	v_and_b32_e32 v39, 0xffffff80, v65
	v_min_f32_e32 v65, v48, v24
	v_max3_f32 v9, v9, v48, v24
	v_max3_f32 v24, v42, v49, v30
	v_add_f32_e32 v27, v27, v28
	v_add_f32_e32 v28, v20, v17
	v_add_f32_e32 v42, v20, v18
	v_add_f32_e32 v20, v20, v26
	v_and_b32_e32 v22, 0xffffff80, v73
	v_and_or_b32 v27, v27, s3, 51
	v_and_or_b32 v28, v28, s3, 64
	v_and_b32_e32 v42, 0xffffff00, v42
	v_and_b32_e32 v20, 0xffffff00, v20
	v_and_b32_e32 v29, 0xffffff80, v74
	v_and_b32_e32 v31, 0xffffff80, v75
	v_and_b32_e32 v33, 0xffffff80, v70
	v_and_b32_e32 v35, 0xffffff80, v71
	v_and_b32_e32 v37, 0xffffff80, v64
; __device__ __forceinline__ void sort16_desc(float (&v)[16]) {
;     CE(v[0], v[1]); CE(v[2], v[3]); CE(v[0], v[2]); CE(v[1], v[3]);
;     CE(v[1], v[2]); CE(v[4], v[5]); CE(v[6], v[7]); CE(v[4], v[6]);
;     CE(v[5], v[7]); CE(v[5], v[6]); CE(v[0], v[4]); CE(v[2], v[6]);
;     CE(v[2], v[4]); CE(v[1], v[5]); CE(v[3], v[7]); CE(v[3], v[5]);
;     CE(v[1], v[2]); CE(v[3], v[4]); CE(v[5], v[6]); CE(v[8], v[9]);
;     __device__ __forceinline__ void fused(f32x4 (&acc)[2][2][4][2], const Unit& u, int wr, int wc, int fr, int fq, PG8_LAS unsigned char* lds, int wid, int lane) const {
;     ...
;             { float cv[16]; cv[0] = __uint_as_float((__float_as_uint(v0[3] + v1[3]) & ~255u) | 51u); cv[1] = __uint_as_float((__float_as_uint(v0[4] + v1[0]) & ~255u) | 64u); cv[2] = __uint_as_float((__float_as_uint(v0[4] + v1[1]) & ~255u) | 65u); cv[3] = __uint_as_float((__float_as_uint(v0[4] + v1[2]) & ~255u) | 66u); cv[4] = __uint_as_float((__float_as_uint(v0[5] + v1[0]) & ~255u) | 80u); cv[5] = __uint_as_float((__float_as_uint(v0[5] + v1[1]) & ~255u) | 81u); cv[6] = __uint_as_float((__float_as_uint(v0[6] + v1[0]) & ~255u) | 96u); cv[7] = __uint_as_float((__float_as_uint(v0[6] + v1[1]) & ~255u) | 97u); cv[8] = __uint_as_float((__float_as_uint(v0[7] + v1[0]) & ~255u) | 112u); cv[9] = __uint_as_float((__float_as_uint(v0[7] + v1[1]) & ~255u) | 113u); cv[10] = __uint_as_float((__float_as_uint(v0[8] + v1[0]) & ~255u) | 128u); cv[11] = __uint_as_float((__float_as_uint(v0[9] + v1[0]) & ~255u) | 144u); cv[12] = __uint_as_float((__float_as_uint(v0[10] + v1[0]) & ~255u) | 160u); cv[13] = __uint_as_float((__float_as_uint(v0[11] + v1[0]) & ~255u) | 176u); cv[14] = __uint_as_float((__float_as_uint(v0[12] + v1[0]) & ~255u) | 192u); cv[15] = __uint_as_float((__float_as_uint(v0[13] + v1[0]) & ~255u) | 208u); sort16_desc(cv); merge_top16(best, cv); }
;             { float cv[16]; cv[0] = __uint_as_float((__float_as_uint(v0[14] + v1[0]) & ~255u) | 224u); cv[1] = __uint_as_float((__float_as_uint(v0[15] + v1[0]) & ~255u) | 240u); cv[2] = -INFINITY; cv[3] = -INFINITY; cv[4] = -INFINITY; cv[5] = -INFINITY; cv[6] = -INFINITY; cv[7] = -INFINITY; cv[8] = -INFINITY; cv[9] = -INFINITY; cv[10] = -INFINITY; cv[11] = -INFINITY; cv[12] = -INFINITY; cv[13] = -INFINITY; cv[14] = -INFINITY; cv[15] = -INFINITY; sort16_desc(cv); merge_top16(best, cv); }
	v_min_f32_e32 v43, v15, v41
	v_min_f32_e32 v44, v19, v10
	v_min_f32_e32 v62, v54, v25
	v_or_b32_e32 v42, 0x41, v42
	v_or_b32_e32 v20, 0x42, v20
	v_add_f32_e32 v26, v22, v17
	v_add_f32_e32 v22, v22, v18
	v_min_f32_e32 v63, v23, v53
	v_max3_f32 v23, v43, v23, v53
	v_max3_f32 v10, v19, v10, v62
	v_max3_f32 v19, v44, v54, v25
	v_and_b32_e32 v26, 0xffffff00, v26
	v_and_b32_e32 v22, 0xffffff00, v22
	v_add_f32_e32 v43, v29, v17
	v_add_f32_e32 v29, v29, v18
	v_add_f32_e32 v44, v31, v17
	v_add_f32_e32 v18, v31, v18
	v_add_f32_e32 v31, v33, v17
	v_add_f32_e32 v33, v35, v17
	v_add_f32_e32 v35, v37, v17
	v_add_f32_e32 v37, v39, v17
	v_max_f32_e32 v39, v27, v28
	v_min_f32_e32 v27, v27, v28
	v_max_f32_e32 v28, v42, v42
	v_or_b32_e32 v26, 0x50, v26
	v_or_b32_e32 v22, 0x51, v22
	v_and_b32_e32 v43, 0xffffff00, v43
	v_and_b32_e32 v29, 0xffffff00, v29
	v_max_f32_e32 v42, v28, v20
	v_min_f32_e32 v20, v28, v20
	v_or_b32_e32 v43, 0x60, v43
	v_or_b32_e32 v29, 0x61, v29
	v_max_f32_e32 v28, v39, v42
	v_min_f32_e32 v39, v39, v42
	v_max_f32_e32 v42, v27, v20
	v_min_f32_e32 v20, v27, v20
	v_max_f32_e32 v27, v42, v39
	v_min_f32_e32 v39, v42, v39
	v_max_f32_e32 v42, v26, v22
	v_min_f32_e32 v22, v26, v22
	v_max_f32_e32 v26, v29, v29
	v_max_f32_e32 v29, v43, v43
	v_max_f32_e32 v43, v29, v26
	v_min_f32_e32 v26, v29, v26
	v_max_f32_e32 v29, v42, v43
	v_min_f32_e32 v42, v42, v43
	v_max_f32_e32 v43, v22, v26
	v_and_b32_e32 v12, 0xffffff80, v68
	v_and_b32_e32 v14, 0xffffff80, v69
	v_min_f32_e32 v22, v22, v26
	v_max_f32_e32 v26, v43, v42
	v_min_f32_e32 v42, v43, v42
	v_add_f32_e32 v12, v12, v17
	v_add_f32_e32 v14, v14, v17
	v_max_f32_e32 v43, v28, v29
	v_min_f32_e32 v28, v28, v29
	v_max_f32_e32 v29, v39, v42
	v_and_b32_e32 v44, 0xffffff00, v44
	v_and_b32_e32 v18, 0xffffff00, v18
	v_and_b32_e32 v12, 0xffffff00, v12
	v_and_b32_e32 v14, 0xffffff00, v14
	v_min_f32_e32 v39, v39, v42
	v_max_f32_e32 v42, v29, v28
	v_min_f32_e32 v28, v29, v28
	v_max_f32_e32 v29, v27, v26
	v_min_f32_e32 v26, v27, v26
	v_max_f32_e32 v27, v20, v22
	v_or_b32_e32 v44, 0x70, v44
	v_or_b32_e32 v18, 0x71, v18
	v_or_b32_e32 v12, 0x80, v12
	v_or_b32_e32 v14, 0x90, v14
	v_min_f32_e32 v20, v20, v22
	v_max_f32_e32 v22, v27, v26
	v_min_f32_e32 v26, v27, v26
	v_and_b32_e32 v31, 0xffffff00, v31
	v_and_b32_e32 v33, 0xffffff00, v33
	v_max_f32_e32 v27, v29, v42
	v_min_f32_e32 v29, v29, v42
	v_max_f32_e32 v42, v22, v28
	v_min_f32_e32 v22, v22, v28
	v_max_f32_e32 v28, v26, v39
	v_min_f32_e32 v26, v26, v39
	v_max_f32_e32 v39, v44, v44
	v_or_b32_e32 v31, 0xa0, v31
	v_or_b32_e32 v33, 0xb0, v33
	v_and_b32_e32 v35, 0xffffff00, v35
	v_and_b32_e32 v37, 0xffffff00, v37
	v_max_f32_e32 v44, v39, v18
	v_min_f32_e32 v18, v39, v18
	v_max_f32_e32 v39, v12, v14
	v_min_f32_e32 v12, v12, v14
	v_or_b32_e32 v35, 0xc0, v35
	v_or_b32_e32 v37, 0xd0, v37
	v_max_f32_e32 v14, v44, v39
	v_min_f32_e32 v39, v44, v39
	v_max_f32_e32 v44, v18, v12
	v_min_f32_e32 v12, v18, v12
	v_max_f32_e32 v18, v44, v39
	v_min_f32_e32 v39, v44, v39
	v_max_f32_e32 v44, v31, v33
	v_min_f32_e32 v31, v31, v33
	v_max_f32_e32 v33, v37, v37
	v_max_f32_e32 v37, v35, v33
	v_min_f32_e32 v33, v35, v33
	v_max_f32_e32 v35, v44, v37
	v_min_f32_e32 v37, v44, v37
	v_max_f32_e32 v44, v31, v33
	v_min_f32_e32 v31, v31, v33
	v_max_f32_e32 v33, v44, v37
	v_min_f32_e32 v37, v44, v37
	v_max_f32_e32 v44, v14, v35
	v_min_f32_e32 v14, v14, v35
	v_max_f32_e32 v35, v39, v37
	v_min_f32_e32 v37, v39, v37
	v_max_f32_e32 v39, v35, v14
	v_min_f32_e32 v14, v35, v14
	v_max_f32_e32 v35, v18, v33
	v_min_f32_e32 v18, v18, v33
	v_max_f32_e32 v33, v12, v31
	v_min_f32_e32 v12, v12, v31
	v_max_f32_e32 v31, v33, v18
	v_min_f32_e32 v45, v5, v11
	v_min_f32_e32 v61, v51, v59
	v_min_f32_e32 v18, v33, v18
	v_max_f32_e32 v33, v35, v39
	v_min_f32_e32 v35, v35, v39
	v_max_f32_e32 v39, v31, v14
	v_min_f32_e32 v14, v31, v14
	v_max3_f32 v5, v5, v11, v61
	v_max3_f32 v11, v45, v51, v59
	v_max_f32_e32 v31, v18, v37
	v_min_f32_e32 v18, v18, v37
	v_min_f32_e32 v37, v43, v44
	v_max_f32_e32 v45, v22, v14
	v_min_f32_e32 v14, v22, v14
	v_max_f32_e32 v22, v45, v37
	v_min_f32_e32 v37, v45, v37
	v_max_f32_e32 v45, v29, v35
	v_min_f32_e32 v29, v29, v35
	v_max_f32_e32 v35, v26, v18
	v_min_f32_e32 v46, v7, v4
	v_min_f32_e32 v47, v6, v3
	v_min_f32_e32 v52, v50, v55
	v_min_f32_e32 v60, v56, v32
	v_min_f32_e32 v64, v49, v30
	v_min_f32_e32 v18, v26, v18
	v_max_f32_e32 v26, v35, v29
	v_min_f32_e32 v29, v35, v29
	v_max3_f32 v21, v40, v38, v21
	v_max3_f32 v8, v8, v34, v65
	v_max3_f32 v13, v36, v13, v64
	v_max3_f32 v15, v15, v41, v63
	v_max3_f32 v4, v7, v4, v60
	v_max3_f32 v7, v46, v56, v32
	v_max3_f32 v3, v6, v3, v52
	v_max3_f32 v6, v47, v50, v55
	v_max3_f32 v2, v2, v58, v57
	v_max_f32_e32 v35, v45, v22
	v_min_f32_e32 v22, v45, v22
	v_max_f32_e32 v45, v26, v37
	v_min_f32_e32 v26, v26, v37
	v_max_f32_e32 v37, v29, v14
	v_min_f32_e32 v14, v29, v14
	v_max_f32_e32 v29, v27, v33
	v_min_f32_e32 v27, v27, v33
	v_max_f32_e32 v33, v28, v31
	v_max_f32_e32 v25, v21, v19
	v_min_f32_e32 v19, v21, v19
	v_max_f32_e32 v21, v8, v5
	v_min_f32_e32 v5, v8, v5
	v_max_f32_e32 v8, v9, v11
	v_min_f32_e32 v9, v9, v11
	v_max_f32_e32 v11, v13, v4
	v_min_f32_e32 v4, v13, v4
	v_max_f32_e32 v13, v24, v7
	v_min_f32_e32 v7, v24, v7
	v_max_f32_e32 v24, v15, v3
	v_min_f32_e32 v3, v15, v3
	v_max_f32_e32 v15, v23, v6
	v_min_f32_e32 v6, v23, v6
	v_max_f32_e32 v23, v10, v2
	v_min_f32_e32 v2, v10, v2
	v_min_f32_e32 v28, v28, v31
	v_max_f32_e32 v31, v33, v27
	v_min_f32_e32 v27, v33, v27
	v_max_f32_e32 v33, v42, v39
	v_min_f32_e32 v39, v42, v39
	v_max_f32_e32 v42, v20, v12
	v_max_f32_e32 v10, v25, v13
	v_min_f32_e32 v13, v25, v13
	v_max_f32_e32 v25, v21, v24
	v_min_f32_e32 v21, v21, v24
; __device__ __forceinline__ void merge_top16(float (&v)[16], const float (&nw)[16]) {
;     v[0] = fmaxf(v[0], nw[15]); v[1] = fmaxf(v[1], nw[14]); v[2] = fmaxf(v[2], nw[13]); v[3] = fmaxf(v[3], nw[12]); v[4] = fmaxf(v[4], nw[11]); v[5] = fmaxf(v[5], nw[10]); v[6] = fmaxf(v[6], nw[9]); v[7] = fmaxf(v[7], nw[8]); v[8] = fmaxf(v[8], nw[7]); v[9] = fmaxf(v[9], nw[6]); v[10] = fmaxf(v[10], nw[5]); v[11] = fmaxf(v[11], nw[4]); v[12] = fmaxf(v[12], nw[3]); v[13] = fmaxf(v[13], nw[2]); v[14] = fmaxf(v[14], nw[1]); v[15] = fmaxf(v[15], nw[0]);
;     CE(v[0], v[8]); CE(v[1], v[9]); CE(v[2], v[10]); CE(v[3], v[11]);
;     CE(v[4], v[12]); CE(v[5], v[13]); CE(v[6], v[14]); CE(v[7], v[15]);
;     CE(v[0], v[4]); CE(v[1], v[5]); CE(v[2], v[6]); CE(v[3], v[7]);
;     CE(v[8], v[12]); CE(v[9], v[13]); CE(v[10], v[14]); CE(v[11], v[15]);
;     CE(v[0], v[2]); CE(v[1], v[3]); CE(v[4], v[6]); CE(v[5], v[7]);
;     CE(v[8], v[10]); CE(v[9], v[11]); CE(v[12], v[14]); CE(v[13], v[15]);
;     __device__ __forceinline__ void fused(f32x4 (&acc)[2][2][4][2], const Unit& u, int wr, int wc, int fr, int fq, PG8_LAS unsigned char* lds, int wid, int lane) const {
;     ...
;             { float cv[16]; cv[0] = __uint_as_float((__float_as_uint(v0[14] + v1[0]) & ~255u) | 224u); cv[1] = __uint_as_float((__float_as_uint(v0[15] + v1[0]) & ~255u) | 240u); cv[2] = -INFINITY; cv[3] = -INFINITY; cv[4] = -INFINITY; cv[5] = -INFINITY; cv[6] = -INFINITY; cv[7] = -INFINITY; cv[8] = -INFINITY; cv[9] = -INFINITY; cv[10] = -INFINITY; cv[11] = -INFINITY; cv[12] = -INFINITY; cv[13] = -INFINITY; cv[14] = -INFINITY; cv[15] = -INFINITY; sort16_desc(cv); merge_top16(best, cv); }
;             float sc[16], sum = 0.f;
; #pragma unroll
;             for (int q = 0; q < 16; ++q) { sc[q] = __uint_as_float(__float_as_uint(best[q]) & ~255u); }
;             const float smax = sc[0];
; #pragma unroll
;             for (int q = 0; q < 16; ++q) { sc[q] = __builtin_amdgcn_exp2f((sc[q] - smax) * 1.4426950408889634f); }
; #pragma unroll
;             for (int q = 0; q < 16; ++q) sum += sc[q];
;             const float rs = 1.0f / sum;
;             asm volatile("s_waitcnt lgkmcnt(0)" ::: "memory");
;             int ex[16];
; #pragma unroll
;             for (int q = 0; q < 16; ++q) { const unsigned cid = __float_as_uint(best[q]) & 255u; ex[q] = idxl[cid >> 4] * 128 + idxl[16 + (cid & 15u)]; }
	v_max_f32_e32 v24, v8, v15
	v_min_f32_e32 v8, v8, v15
	v_max_f32_e32 v15, v11, v23
	v_min_f32_e32 v11, v11, v23
	v_max_f32_e32 v23, v19, v7
	v_min_f32_e32 v7, v19, v7
	v_max_f32_e32 v19, v5, v3
	v_min_f32_e32 v3, v5, v3
	v_max_f32_e32 v5, v9, v6
	v_min_f32_e32 v6, v9, v6
	v_max_f32_e32 v9, v4, v2
	v_min_f32_e32 v2, v4, v2
	v_min_f32_e32 v12, v20, v12
	v_max_f32_e32 v20, v42, v39
	v_min_f32_e32 v39, v42, v39
	v_and_b32_e32 v1, 0xffffff80, v66
	v_and_b32_e32 v0, 0xffffff80, v67
	v_max_f32_e32 v4, v10, v24
	v_min_f32_e32 v10, v10, v24
	v_max_f32_e32 v24, v25, v15
	v_min_f32_e32 v15, v25, v15
	v_max_f32_e32 v25, v13, v8
	v_min_f32_e32 v8, v13, v8
	v_max_f32_e32 v13, v21, v11
	v_min_f32_e32 v11, v21, v11
	v_max_f32_e32 v21, v23, v5
	v_min_f32_e32 v5, v23, v5
	v_max_f32_e32 v23, v19, v9
	v_min_f32_e32 v9, v19, v9
	v_max_f32_e32 v19, v7, v6
	v_min_f32_e32 v6, v7, v6
	v_max_f32_e32 v7, v3, v2
	v_min_f32_e32 v2, v3, v2
	v_max_f32_e32 v42, v33, v31
	v_min_f32_e32 v31, v33, v31
	v_max_f32_e32 v33, v20, v27
	v_min_f32_e32 v20, v20, v27
	v_max_f32_e32 v27, v39, v28
	v_min_f32_e32 v28, v39, v28
	v_min_f32_e32 v3, v4, v24
	v_min_f32_e32 v30, v10, v15
	v_min_f32_e32 v32, v25, v13
	v_min_f32_e32 v34, v8, v11
	v_min_f32_e32 v36, v21, v23
	v_min_f32_e32 v38, v5, v9
	v_min_f32_e32 v40, v19, v7
	v_min_f32_e32 v41, v6, v2
	v_max_f32_e32 v39, v29, v35
	v_min_f32_e32 v29, v29, v35
	v_max_f32_e32 v35, v42, v22
	v_min_f32_e32 v22, v42, v22
	v_max_f32_e32 v42, v31, v45
	v_min_f32_e32 v31, v31, v45
	v_max_f32_e32 v45, v33, v26
	v_min_f32_e32 v26, v33, v26
	v_max_f32_e32 v33, v20, v37
	v_min_f32_e32 v20, v20, v37
	v_max_f32_e32 v37, v27, v14
	v_min_f32_e32 v14, v27, v14
	v_max_f32_e32 v27, v28, v18
	v_min_f32_e32 v18, v28, v18
	v_add_f32_e32 v1, v1, v17
	v_add_f32_e32 v0, v0, v17
	v_max3_f32 v4, v4, v24, v12
	v_max_f32_e32 v3, v3, v18
	v_max3_f32 v10, v10, v15, v27
	v_max_f32_e32 v12, v30, v14
	v_max3_f32 v13, v25, v13, v37
	v_max_f32_e32 v14, v32, v20
	v_max3_f32 v8, v8, v11, v33
	v_max_f32_e32 v11, v34, v26
	v_max3_f32 v15, v21, v23, v45
	v_max_f32_e32 v18, v36, v31
	v_max3_f32 v5, v5, v9, v42
	v_max_f32_e32 v9, v38, v22
	v_max3_f32 v7, v19, v7, v35
	v_max_f32_e32 v19, v40, v29
	v_max3_f32 v2, v6, v2, v39
	v_max3_f32 v6, v41, v43, v44
	v_and_b32_e32 v1, 0xffffff00, v1
	v_and_b32_e32 v0, 0xffffff00, v0
	v_max_f32_e32 v20, v4, v15
	v_min_f32_e32 v4, v4, v15
	v_max_f32_e32 v15, v3, v18
	v_min_f32_e32 v3, v3, v18
	v_max_f32_e32 v18, v10, v5
	v_min_f32_e32 v5, v10, v5
	v_max_f32_e32 v10, v12, v9
	v_min_f32_e32 v9, v12, v9
	v_max_f32_e32 v12, v13, v7
	v_min_f32_e32 v7, v13, v7
	v_max_f32_e32 v13, v14, v19
	v_min_f32_e32 v14, v14, v19
	v_max_f32_e32 v19, v8, v2
	v_min_f32_e32 v2, v8, v2
	v_max_f32_e32 v8, v11, v6
	v_min_f32_e32 v6, v11, v6
	v_or_b32_e32 v1, 0xe0, v1
	v_or_b32_e32 v0, 0xf0, v0
	v_max_f32_e32 v11, v20, v12
	v_min_f32_e32 v12, v20, v12
	v_max_f32_e32 v20, v15, v13
	v_min_f32_e32 v13, v15, v13
	v_max_f32_e32 v15, v18, v19
	v_min_f32_e32 v18, v18, v19
	v_max_f32_e32 v19, v10, v8
	v_min_f32_e32 v8, v10, v8
	v_max_f32_e32 v10, v4, v7
	v_min_f32_e32 v4, v4, v7
	v_max_f32_e32 v7, v3, v14
	v_min_f32_e32 v3, v3, v14
	v_max_f32_e32 v14, v5, v2
	v_min_f32_e32 v2, v5, v2
	v_max_f32_e32 v5, v9, v6
	v_min_f32_e32 v6, v9, v6
	v_max_f32_e32 v9, v11, v15
	v_min_f32_e32 v11, v11, v15
	v_max_f32_e32 v15, v20, v19
	v_min_f32_e32 v19, v20, v19
	v_max_f32_e32 v20, v12, v18
	v_min_f32_e32 v12, v12, v18
	v_max_f32_e32 v18, v13, v8
	v_min_f32_e32 v8, v13, v8
	v_max_f32_e32 v13, v10, v14
	v_min_f32_e32 v10, v10, v14
	v_max_f32_e32 v14, v7, v5
	v_min_f32_e32 v5, v7, v5
	v_max_f32_e32 v7, v4, v2
	v_min_f32_e32 v2, v4, v2
	v_max_f32_e32 v4, v3, v6
	v_min_f32_e32 v3, v3, v6
	v_max_f32_e32 v17, v1, v0
	v_min_f32_e32 v0, v1, v0
	v_min_f32_e32 v6, v9, v15
	v_min_f32_e32 v21, v11, v19
	v_min_f32_e32 v22, v20, v18
	v_min_f32_e32 v23, v12, v8
	v_min_f32_e32 v24, v13, v14
	v_min_f32_e32 v25, v10, v5
	v_min_f32_e32 v26, v7, v4
	v_min_f32_e32 v27, v2, v3
	s_mov_b32 s3, 0xff800000
	v_max_f32_e32 v0, 0xff800000, v0
	v_max3_f32 v1, v9, v15, s3
	v_max_f32_e32 v6, 0xff800000, v6
	v_max3_f32 v9, v11, v19, s3
	v_max_f32_e32 v11, 0xff800000, v21
	v_max3_f32 v15, v20, v18, s3
	v_max_f32_e32 v18, 0xff800000, v22
	v_max3_f32 v8, v12, v8, s3
	v_max_f32_e32 v12, 0xff800000, v23
	v_max3_f32 v13, v13, v14, s3
	v_max_f32_e32 v14, 0xff800000, v24
	v_max3_f32 v5, v10, v5, s3
	v_max_f32_e32 v10, 0xff800000, v25
	v_max3_f32 v4, v7, v4, s3
	v_max_f32_e32 v7, 0xff800000, v26
	v_max3_f32 v0, v2, v3, v0
	v_max3_f32 v2, v27, v17, s3
	v_max_f32_e32 v3, v1, v13
	v_min_f32_e32 v1, v1, v13
	v_max_f32_e32 v13, v6, v14
	v_min_f32_e32 v6, v6, v14
	v_max_f32_e32 v14, v9, v5
	v_min_f32_e32 v5, v9, v5
	v_max_f32_e32 v9, v11, v10
	v_min_f32_e32 v10, v11, v10
	v_max_f32_e32 v11, v15, v4
	v_min_f32_e32 v4, v15, v4
	v_max_f32_e32 v15, v18, v7
	v_max_f32_e32 v17, v8, v0
	v_min_f32_e32 v0, v8, v0
	v_max_f32_e32 v8, v12, v2
	v_min_f32_e32 v2, v12, v2
	v_max_f32_e32 v12, v3, v11
	v_min_f32_e32 v3, v3, v11
	v_max_f32_e32 v11, v13, v15
	v_min_f32_e32 v13, v13, v15
	v_max_f32_e32 v15, v14, v17
	v_min_f32_e32 v14, v14, v17
	v_max_f32_e32 v17, v9, v8
	v_min_f32_e32 v8, v9, v8
	v_max_f32_e32 v9, v1, v4
	v_min_f32_e32 v24, v1, v4
	v_max_f32_e32 v27, v5, v0
	v_min_f32_e32 v28, v5, v0
	v_max_f32_e32 v29, v10, v2
	v_min_f32_e32 v30, v10, v2
	v_max_f32_e32 v0, v12, v15
	v_min_f32_e32 v1, v12, v15
	v_max_f32_e32 v2, v11, v17
	v_min_f32_e32 v4, v11, v17
	v_min_f32_e32 v7, v18, v7
	v_max_f32_e32 v33, v0, v2
	v_min_f32_e32 v34, v0, v2
	v_min_f32_e32 v36, v1, v4
	v_max_f32_e32 v25, v6, v7
	v_min_f32_e32 v26, v6, v7
	v_max_f32_e32 v35, v1, v4
	v_lshrrev_b32_e32 v0, 2, v33
	v_lshrrev_b32_e32 v2, 2, v34
	v_lshrrev_b32_e32 v6, 2, v36
	v_max_f32_e32 v17, v3, v14
	v_min_f32_e32 v31, v3, v14
	v_and_b32_e32 v0, 60, v0
	v_and_b32_e32 v1, 15, v33
	v_and_b32_e32 v2, 60, v2
	v_and_b32_e32 v3, 15, v34
	v_lshrrev_b32_e32 v4, 2, v35
	v_and_b32_e32 v5, 15, v35
	v_and_b32_e32 v6, 60, v6
	v_and_b32_e32 v7, 15, v36
	s_waitcnt lgkmcnt(0)
; #define RT_PK(q_) (ex[q_] | (int)((__float_as_uint(usc[ex[q_]]) >> 23) << 14))
;     __device__ __forceinline__ void fused(f32x4 (&acc)[2][2][4][2], const Unit& u, int wr, int wc, int fr, int fq, PG8_LAS unsigned char* lds, int wid, int lane) const {
;     ...
;             for (int q = 0; q < 16; ++q) { sc[q] = __uint_as_float(__float_as_uint(best[q]) & ~255u); }
;             const float smax = sc[0];
; #pragma unroll
;             for (int q = 0; q < 16; ++q) { sc[q] = __builtin_amdgcn_exp2f((sc[q] - smax) * 1.4426950408889634f); }
; #pragma unroll
;             for (int q = 0; q < 16; ++q) sum += sc[q];
;             const float rs = 1.0f / sum;
;             asm volatile("s_waitcnt lgkmcnt(0)" ::: "memory");
;             int ex[16];
; #pragma unroll
;             for (int q = 0; q < 16; ++q) { const unsigned cid = __float_as_uint(best[q]) & 255u; ex[q] = idxl[cid >> 4] * 128 + idxl[16 + (cid & 15u)]; }
;             const size_t o = ((size_t)u.pn * 16384 + (size_t)(u.pm * BM + row)) * 16;
;             typedef int i32x4 __attribute__((ext_vector_type(4)));
; #pragma unroll
;             for (int i = 0; i < 4; ++i) {
;     ...
;                 *(i32x4*)(eidx + o + 4 * i) = (i32x4){RT_PK(4 * i), RT_PK(4 * i + 1), RT_PK(4 * i + 2), RT_PK(4 * i + 3)};
	v_add_u32_e32 v0, v16, v0
	v_lshl_add_u32 v1, v1, 2, v16
	v_add_u32_e32 v2, v16, v2
	v_lshl_add_u32 v3, v3, 2, v16
	v_and_b32_e32 v4, 60, v4
	v_lshl_add_u32 v5, v5, 2, v16
	v_add_u32_e32 v6, v16, v6
	v_lshl_add_u32 v7, v7, 2, v16
	v_add_u32_e32 v4, v16, v4
	ds_read_b32 v0, v0
	ds_read_b32 v1, v1 offset:64
	ds_read_b32 v2, v2
	ds_read_b32 v3, v3 offset:64
	ds_read_b32 v10, v4
	ds_read_b32 v5, v5 offset:64
	ds_read_b32 v6, v6
	ds_read_b32 v7, v7 offset:64
	s_waitcnt lgkmcnt(0)
	v_lshl_add_u32 v0, v0, 7, v1
	v_ashrrev_i32_e32 v1, 31, v0
	v_lshl_add_u32 v4, v2, 7, v3
	v_lshlrev_b64 v[14:15], 3, v[0:1]
	v_lshl_add_u32 v10, v10, 7, v5
	v_lshl_add_u32 v12, v6, 7, v7
	v_lshl_add_u64 v[2:3], s[8:9], 0, v[14:15]
	v_ashrrev_i32_e32 v5, 31, v4
	v_max_f32_e32 v32, v13, v8
	v_min_f32_e32 v8, v13, v8
	global_load_dwordx2 v[170:171], v[2:3], off
	v_lshlrev_b64 v[18:19], 3, v[4:5]
	v_ashrrev_i32_e32 v11, 31, v10
	v_ashrrev_i32_e32 v13, 31, v12
	v_lshl_add_u64 v[2:3], s[8:9], 0, v[18:19]
	v_lshlrev_b64 v[20:21], 3, v[10:11]
	v_lshlrev_b64 v[22:23], 3, v[12:13]
	v_lshl_add_u64 v[6:7], s[8:9], 0, v[20:21]
	global_load_dwordx2 v[172:173], v[2:3], off
	global_load_dwordx2 v[174:175], v[6:7], off
	v_lshl_add_u64 v[2:3], s[8:9], 0, v[22:23]
	global_load_dwordx2 v[176:177], v[2:3], off
	v_min_f32_e32 v2, v9, v27
	v_min_f32_e32 v6, v25, v29
	v_max_f32_e32 v43, v2, v6
	v_min_f32_e32 v44, v2, v6
	v_and_b32_e32 v2, 0xffffff00, v34
	v_and_b32_e32 v51, 0xffffff00, v33
	v_max_f32_e32 v37, v9, v27
	v_max_f32_e32 v3, v25, v29
	v_sub_f32_e32 v2, v2, v51
	v_min_f32_e32 v9, v24, v28
	v_min_f32_e32 v25, v26, v30
	v_max_f32_e32 v41, v37, v3
	v_min_f32_e32 v42, v37, v3
	v_and_b32_e32 v3, 0xffffff00, v35
	v_mul_f32_e32 v2, 0x3fb8aa3b, v2
	v_max_f32_e32 v47, v9, v25
	v_min_f32_e32 v48, v9, v25
	v_exp_f32_e32 v25, v2
	v_sub_f32_e32 v2, v3, v51
	v_and_b32_e32 v6, 0xffffff00, v36
	v_mul_f32_e32 v2, 0x3fb8aa3b, v2
	v_max_f32_e32 v7, v24, v28
	v_max_f32_e32 v24, v26, v30
	v_max_f32_e32 v38, v17, v32
	v_exp_f32_e32 v26, v2
	v_sub_f32_e32 v2, v6, v51
	v_max_f32_e32 v45, v7, v24
	v_min_f32_e32 v46, v7, v24
	v_and_b32_e32 v7, 0xffffff00, v38
	v_mul_f32_e32 v2, 0x3fb8aa3b, v2
	v_min_f32_e32 v17, v17, v32
	v_exp_f32_e32 v27, v2
	v_sub_f32_e32 v2, v7, v51
	v_max_f32_e32 v39, v31, v8
	v_min_f32_e32 v40, v31, v8
	v_and_b32_e32 v8, 0xffffff00, v17
	v_mul_f32_e32 v2, 0x3fb8aa3b, v2
	v_exp_f32_e32 v28, v2
	v_sub_f32_e32 v2, v8, v51
	v_and_b32_e32 v9, 0xffffff00, v39
	v_mul_f32_e32 v2, 0x3fb8aa3b, v2
	v_exp_f32_e32 v29, v2
	v_sub_f32_e32 v2, v9, v51
	v_and_b32_e32 v31, 0xffffff00, v40
	v_mul_f32_e32 v2, 0x3fb8aa3b, v2
	v_exp_f32_e32 v30, v2
	v_sub_f32_e32 v2, v31, v51
	v_and_b32_e32 v32, 0xffffff00, v41
	v_mul_f32_e32 v2, 0x3fb8aa3b, v2
	v_exp_f32_e32 v31, v2
	v_sub_f32_e32 v2, v32, v51
	v_and_b32_e32 v34, 0xffffff00, v42
	v_mul_f32_e32 v2, 0x3fb8aa3b, v2
	v_exp_f32_e32 v6, v2
	v_sub_f32_e32 v2, v34, v51
	v_and_b32_e32 v35, 0xffffff00, v43
	v_mul_f32_e32 v2, 0x3fb8aa3b, v2
	v_exp_f32_e32 v7, v2
	v_sub_f32_e32 v2, v35, v51
	v_mul_f32_e32 v2, 0x3fb8aa3b, v2
	v_exp_f32_e32 v8, v2
	v_lshl_or_b32 v2, s18, 8, v128
	v_ashrrev_i32_e32 v3, 31, v2
	s_lshl_b64 s[4:5], s[16:17], 18
	s_mov_b32 s3, 0x7fc000
	v_lshl_add_u64 v[32:33], v[2:3], 4, s[4:5]
	v_sub_f32_e32 v24, v51, v51
	v_mul_f32_e32 v24, 0x3fb8aa3b, v24
	v_exp_f32_e32 v24, v24
	s_waitcnt vmcnt(0)
	v_lshrrev_b32_e32 v1, 9, v170
	v_and_or_b32 v2, v1, s3, v0
	v_and_b32_e32 v36, 0xffffff00, v44
	v_and_b32_e32 v37, 0xffffff00, v45
	v_and_b32_e32 v49, 0xffffff00, v46
	v_and_b32_e32 v50, 0xffffff00, v47
	v_and_b32_e32 v52, 0xffffff00, v48
	v_lshrrev_b32_e32 v0, 9, v172
	v_and_or_b32 v3, v0, s3, v4
	v_lshrrev_b32_e32 v0, 9, v174
	v_and_or_b32 v4, v0, s3, v10
	v_lshrrev_b32_e32 v0, 9, v176
	v_and_or_b32 v5, v0, s3, v12
	v_lshlrev_b64 v[12:13], 2, v[32:33]
	v_lshl_add_u64 v[0:1], s[12:13], 0, v[12:13]
	s_nop 0
	v_readfirstlane_b32 s98, v0
	v_readfirstlane_b32 s99, v1
	v_lshrrev_b32_e32 v202, 6, v128
	v_and_b32_e32 v203, 63, v128
	v_lshlrev_b32_e32 v202, 13, v202
	v_lshl_or_b32 v204, v203, 6, v202
	v_lshl_or_b32 v205, v203, 4, v202
	v_lshlrev_b32_e32 v203, 4, v203
	ds_write_b128 v204, v[2:5]
	v_lshrrev_b32_e32 v32, 2, v40
	v_add_f32_e32 v10, 0, v24
	v_add_f32_e32 v10, v25, v10
	v_add_f32_e32 v10, v26, v10
	v_add_f32_e32 v10, v27, v10
	v_sub_f32_e32 v2, v36, v51
	v_add_f32_e32 v10, v28, v10
	v_mul_f32_e32 v2, 0x3fb8aa3b, v2
	v_add_f32_e32 v10, v29, v10
	v_exp_f32_e32 v9, v2
	v_sub_f32_e32 v2, v37, v51
	v_add_f32_e32 v10, v30, v10
	v_mul_f32_e32 v2, 0x3fb8aa3b, v2
	v_sub_f32_e32 v3, v49, v51
	v_add_f32_e32 v10, v31, v10
	v_exp_f32_e32 v2, v2
	v_mul_f32_e32 v3, 0x3fb8aa3b, v3
	v_sub_f32_e32 v4, v50, v51
	v_add_f32_e32 v10, v6, v10
	v_exp_f32_e32 v3, v3
	v_mul_f32_e32 v4, 0x3fb8aa3b, v4
	v_sub_f32_e32 v5, v52, v51
	v_add_f32_e32 v10, v7, v10
	v_exp_f32_e32 v4, v4
	v_mul_f32_e32 v5, 0x3fb8aa3b, v5
	v_add_f32_e32 v10, v8, v10
	v_exp_f32_e32 v5, v5
	v_add_f32_e32 v10, v9, v10
	v_add_f32_e32 v10, v2, v10
	v_lshrrev_b32_e32 v11, 2, v38
	v_lshrrev_b32_e32 v15, 2, v17
	v_add_f32_e32 v10, v3, v10
	v_and_b32_e32 v11, 60, v11
	v_and_b32_e32 v14, 15, v38
	v_and_b32_e32 v15, 60, v15
	v_and_b32_e32 v17, 15, v17
	v_lshrrev_b32_e32 v22, 2, v39
	v_and_b32_e32 v23, 15, v39
	v_and_b32_e32 v33, 15, v40
	v_add_f32_e32 v10, v4, v10
	v_add_u32_e32 v11, v16, v11
	v_lshl_add_u32 v14, v14, 2, v16
	v_add_u32_e32 v15, v16, v15
	v_lshl_add_u32 v17, v17, 2, v16
	v_and_b32_e32 v22, 60, v22
	v_lshl_add_u32 v23, v23, 2, v16
	v_and_b32_e32 v32, 60, v32
	v_lshl_add_u32 v33, v33, 2, v16
	v_add_f32_e32 v10, v5, v10
	v_add_u32_e32 v22, v16, v22
	v_add_u32_e32 v32, v16, v32
	ds_read_b32 v11, v11
	ds_read_b32 v14, v14 offset:64
	ds_read_b32 v15, v15
	ds_read_b32 v17, v17 offset:64
	ds_read_b32 v34, v22
	ds_read_b32 v23, v23 offset:64
	ds_read_b32 v35, v32
	ds_read_b32 v33, v33 offset:64
	s_waitcnt lgkmcnt(6)
; #define RT_PK(q_) (ex[q_] | (int)((__float_as_uint(usc[ex[q_]]) >> 23) << 14))
;     __device__ __forceinline__ void fused(f32x4 (&acc)[2][2][4][2], const Unit& u, int wr, int wc, int fr, int fq, PG8_LAS unsigned char* lds, int wid, int lane) const {
;     ...
;             const float rs = 1.0f / sum;
;             asm volatile("s_waitcnt lgkmcnt(0)" ::: "memory");
;             int ex[16];
; #pragma unroll
;             for (int q = 0; q < 16; ++q) { const unsigned cid = __float_as_uint(best[q]) & 255u; ex[q] = idxl[cid >> 4] * 128 + idxl[16 + (cid & 15u)]; }
;             const size_t o = ((size_t)u.pn * 16384 + (size_t)(u.pm * BM + row)) * 16;
;             typedef int i32x4 __attribute__((ext_vector_type(4)));
; #pragma unroll
;             for (int i = 0; i < 4; ++i) {
;     ...
;                 *(i32x4*)(eidx + o + 4 * i) = (i32x4){RT_PK(4 * i), RT_PK(4 * i + 1), RT_PK(4 * i + 2), RT_PK(4 * i + 3)};
;                 *(f32x4*)(egate + o + 4 * i) = (f32x4){sc[4 * i] * rs * vsc[ex[4 * i]], sc[4 * i + 1] * rs * vsc[ex[4 * i + 1]], sc[4 * i + 2] * rs * vsc[ex[4 * i + 2]], sc[4 * i + 3] * rs * vsc[ex[4 * i + 3]]};
	v_lshl_add_u32 v14, v11, 7, v14
	v_div_scale_f32 v11, s[4:5], v10, v10, 1.0
	v_rcp_f32_e32 v36, v11
	s_waitcnt lgkmcnt(4)
	v_lshl_add_u32 v22, v15, 7, v17
	s_waitcnt lgkmcnt(2)
	v_lshl_add_u32 v32, v34, 7, v23
	s_waitcnt lgkmcnt(0)
	v_lshl_add_u32 v34, v35, 7, v33
	v_fma_f32 v15, -v11, v36, 1.0
	v_fmac_f32_e32 v36, v15, v36
	v_div_scale_f32 v15, vcc, 1.0, v10, 1.0
	v_mul_f32_e32 v17, v15, v36
	v_fma_f32 v23, -v11, v17, v15
	v_fmac_f32_e32 v17, v23, v36
	v_fma_f32 v11, -v11, v17, v15
	v_div_fmas_f32 v11, v11, v36, v17
	v_div_fixup_f32 v10, v11, v10, 1.0
	v_pk_mul_f32 v[24:25], v[24:25], v[10:11] op_sel_hi:[1,0]
	v_pk_mul_f32 v[26:27], v[26:27], v[10:11] op_sel_hi:[1,0]
	v_ashrrev_i32_e32 v15, 31, v14
	v_ashrrev_i32_e32 v33, 31, v32
	v_lshl_add_u64 v[12:13], s[10:11], 0, v[12:13]
	s_nop 0
	v_readfirstlane_b32 s100, v12
	v_readfirstlane_b32 s101, v13
	v_ashrrev_i32_e32 v23, 31, v22
	v_lshlrev_b64 v[36:37], 3, v[32:33]
	v_lshl_add_u64 v[38:39], s[8:9], 0, v[36:37]
	v_ashrrev_i32_e32 v35, 31, v34
	v_mul_f32_e32 v18, v24, v171
	v_mul_f32_e32 v19, v25, v173
	v_lshlrev_b64 v[24:25], 3, v[14:15]
	v_mul_f32_e32 v20, v26, v175
	v_mul_f32_e32 v21, v27, v177
	ds_write_b128 v204, v[18:21] offset:4096
	v_lshlrev_b64 v[26:27], 3, v[22:23]
	s_nop 0
	v_lshl_add_u64 v[18:19], s[8:9], 0, v[24:25]
	v_lshl_add_u64 v[20:21], s[8:9], 0, v[26:27]
	global_load_dwordx2 v[178:179], v[18:19], off
	global_load_dwordx2 v[180:181], v[20:21], off
	global_load_dwordx2 v[182:183], v[38:39], off
	v_lshlrev_b64 v[38:39], 3, v[34:35]
	v_lshl_add_u64 v[18:19], s[8:9], 0, v[38:39]
	global_load_dwordx2 v[184:185], v[18:19], off
	s_waitcnt vmcnt(3)
	v_lshrrev_b32_e32 v11, 9, v178
	v_and_or_b32 v18, v11, s3, v14
	s_waitcnt vmcnt(2)
	v_lshrrev_b32_e32 v11, 9, v180
	v_and_or_b32 v19, v11, s3, v22
	s_waitcnt vmcnt(1)
	v_lshrrev_b32_e32 v11, 9, v182
	v_and_or_b32 v20, v11, s3, v32
	s_waitcnt vmcnt(0)
	v_lshrrev_b32_e32 v11, 9, v184
	v_and_or_b32 v21, v11, s3, v34
	ds_write_b128 v204, v[18:21] offset:16
	v_lshrrev_b32_e32 v11, 2, v41
	v_lshrrev_b32_e32 v15, 2, v42
	v_lshrrev_b32_e32 v18, 2, v43
	v_lshrrev_b32_e32 v20, 2, v44
	v_and_b32_e32 v11, 60, v11
	v_and_b32_e32 v14, 15, v41
	v_and_b32_e32 v15, 60, v15
	v_and_b32_e32 v17, 15, v42
	v_and_b32_e32 v18, 60, v18
	v_and_b32_e32 v19, 15, v43
	v_and_b32_e32 v20, 60, v20
	v_and_b32_e32 v21, 15, v44
	v_add_u32_e32 v11, v16, v11
	v_lshl_add_u32 v14, v14, 2, v16
	v_add_u32_e32 v15, v16, v15
	v_lshl_add_u32 v17, v17, 2, v16
	v_add_u32_e32 v18, v16, v18
	v_lshl_add_u32 v19, v19, 2, v16
	v_add_u32_e32 v20, v16, v20
	v_lshl_add_u32 v21, v21, 2, v16
	ds_read_b32 v11, v11
	ds_read_b32 v14, v14 offset:64
	ds_read_b32 v15, v15
	ds_read_b32 v17, v17 offset:64
	ds_read_b32 v18, v18
	ds_read_b32 v19, v19 offset:64
	ds_read_b32 v20, v20
	ds_read_b32 v21, v21 offset:64
	s_waitcnt lgkmcnt(6)
	v_lshl_add_u32 v14, v11, 7, v14
	s_waitcnt lgkmcnt(4)
	v_lshl_add_u32 v22, v15, 7, v17
	s_waitcnt lgkmcnt(2)
	v_lshl_add_u32 v32, v18, 7, v19
	v_pk_mul_f32 v[18:19], v[28:29], v[10:11] op_sel_hi:[1,0]
	s_waitcnt lgkmcnt(0)
	v_lshl_add_u32 v34, v20, 7, v21
	v_pk_mul_f32 v[20:21], v[30:31], v[10:11] op_sel_hi:[1,0]
	v_ashrrev_i32_e32 v15, 31, v14
	v_ashrrev_i32_e32 v33, 31, v32
	v_ashrrev_i32_e32 v23, 31, v22
	v_lshlrev_b64 v[28:29], 3, v[32:33]
	v_lshl_add_u64 v[30:31], s[8:9], 0, v[28:29]
	v_ashrrev_i32_e32 v35, 31, v34
	v_mul_f32_e32 v20, v20, v183
	v_mul_f32_e32 v21, v21, v185
	v_mul_f32_e32 v18, v18, v179
	v_mul_f32_e32 v19, v19, v181
	v_lshlrev_b64 v[24:25], 3, v[14:15]
	ds_write_b128 v204, v[18:21] offset:4112
	v_lshlrev_b64 v[26:27], 3, v[22:23]
	s_nop 0
	v_lshl_add_u64 v[18:19], s[8:9], 0, v[24:25]
	v_lshl_add_u64 v[20:21], s[8:9], 0, v[26:27]
	global_load_dwordx2 v[186:187], v[18:19], off
	global_load_dwordx2 v[188:189], v[20:21], off
	global_load_dwordx2 v[190:191], v[30:31], off
	v_lshlrev_b64 v[30:31], 3, v[34:35]
	v_lshl_add_u64 v[18:19], s[8:9], 0, v[30:31]
	global_load_dwordx2 v[192:193], v[18:19], off
	s_waitcnt vmcnt(3)
; #define RT_PK(q_) (ex[q_] | (int)((__float_as_uint(usc[ex[q_]]) >> 23) << 14))
;     __device__ __forceinline__ void fused(f32x4 (&acc)[2][2][4][2], const Unit& u, int wr, int wc, int fr, int fq, PG8_LAS unsigned char* lds, int wid, int lane) const {
;     ...
;             for (int q = 0; q < 16; ++q) { const unsigned cid = __float_as_uint(best[q]) & 255u; ex[q] = idxl[cid >> 4] * 128 + idxl[16 + (cid & 15u)]; }
;             const size_t o = ((size_t)u.pn * 16384 + (size_t)(u.pm * BM + row)) * 16;
;             typedef int i32x4 __attribute__((ext_vector_type(4)));
; #pragma unroll
;             for (int i = 0; i < 4; ++i) {
;     ...
;                 *(i32x4*)(eidx + o + 4 * i) = (i32x4){RT_PK(4 * i), RT_PK(4 * i + 1), RT_PK(4 * i + 2), RT_PK(4 * i + 3)};
;                 *(f32x4*)(egate + o + 4 * i) = (f32x4){sc[4 * i] * rs * vsc[ex[4 * i]], sc[4 * i + 1] * rs * vsc[ex[4 * i + 1]], sc[4 * i + 2] * rs * vsc[ex[4 * i + 2]], sc[4 * i + 3] * rs * vsc[ex[4 * i + 3]]};
	v_lshrrev_b32_e32 v11, 9, v186
	v_and_or_b32 v18, v11, s3, v14
	s_waitcnt vmcnt(2)
	v_lshrrev_b32_e32 v11, 9, v188
	v_and_or_b32 v19, v11, s3, v22
	s_waitcnt vmcnt(1)
	v_lshrrev_b32_e32 v11, 9, v190
	v_and_or_b32 v20, v11, s3, v32
	s_waitcnt vmcnt(0)
	v_lshrrev_b32_e32 v11, 9, v192
	v_and_or_b32 v21, v11, s3, v34
	ds_write_b128 v204, v[18:21] offset:32
	v_lshrrev_b32_e32 v11, 2, v45
	v_lshrrev_b32_e32 v15, 2, v46
	v_lshrrev_b32_e32 v18, 2, v47
	v_lshrrev_b32_e32 v20, 2, v48
	v_and_b32_e32 v11, 60, v11
	v_and_b32_e32 v14, 15, v45
	v_and_b32_e32 v15, 60, v15
	v_and_b32_e32 v17, 15, v46
	v_and_b32_e32 v18, 60, v18
	v_and_b32_e32 v19, 15, v47
	v_and_b32_e32 v20, 60, v20
	v_add_u32_e32 v11, v16, v11
	v_lshl_add_u32 v14, v14, 2, v16
	v_add_u32_e32 v15, v16, v15
	v_lshl_add_u32 v17, v17, 2, v16
	v_add_u32_e32 v18, v16, v18
	v_lshl_add_u32 v19, v19, 2, v16
	v_add_u32_e32 v20, v16, v20
	v_and_b32_e32 v21, 15, v48
	v_lshl_add_u32 v16, v21, 2, v16
	ds_read_b32 v11, v11
	ds_read_b32 v14, v14 offset:64
	ds_read_b32 v15, v15
	ds_read_b32 v17, v17 offset:64
	ds_read_b32 v18, v18
	ds_read_b32 v19, v19 offset:64
	ds_read_b32 v20, v20
	ds_read_b32 v21, v16 offset:64
	s_waitcnt lgkmcnt(6)
	v_lshl_add_u32 v14, v11, 7, v14
	s_waitcnt lgkmcnt(4)
	v_lshl_add_u32 v16, v15, 7, v17
	s_waitcnt lgkmcnt(2)
	v_lshl_add_u32 v18, v18, 7, v19
	v_pk_mul_f32 v[6:7], v[6:7], v[10:11] op_sel_hi:[1,0]
	v_pk_mul_f32 v[8:9], v[8:9], v[10:11] op_sel_hi:[1,0]
	v_ashrrev_i32_e32 v15, 31, v14
	v_ashrrev_i32_e32 v19, 31, v18
	s_waitcnt lgkmcnt(0)
	v_lshl_add_u32 v20, v20, 7, v21
	v_lshlrev_b64 v[22:23], 3, v[14:15]
	v_ashrrev_i32_e32 v17, 31, v16
	v_ashrrev_i32_e32 v21, 31, v20
	v_mul_f32_e32 v8, v8, v191
	v_mul_f32_e32 v9, v9, v193
	v_mul_f32_e32 v6, v6, v187
	v_mul_f32_e32 v7, v7, v189
	v_lshlrev_b64 v[26:27], 3, v[18:19]
	ds_write_b128 v204, v[6:9] offset:4128
	v_lshlrev_b64 v[24:25], 3, v[16:17]
	v_lshl_add_u64 v[28:29], s[8:9], 0, v[26:27]
	v_lshl_add_u64 v[6:7], s[8:9], 0, v[22:23]
	v_lshl_add_u64 v[8:9], s[8:9], 0, v[24:25]
	global_load_dwordx2 v[194:195], v[6:7], off
	global_load_dwordx2 v[196:197], v[8:9], off
	global_load_dwordx2 v[198:199], v[28:29], off
	v_lshlrev_b64 v[28:29], 3, v[20:21]
	v_lshl_add_u64 v[6:7], s[8:9], 0, v[28:29]
	global_load_dwordx2 v[200:201], v[6:7], off
	s_waitcnt vmcnt(3)
	v_lshrrev_b32_e32 v6, 9, v194
	s_waitcnt vmcnt(2)
	v_lshrrev_b32_e32 v7, 9, v196
	s_waitcnt vmcnt(1)
	v_lshrrev_b32_e32 v8, 9, v198
	v_and_or_b32 v6, v6, s3, v14
	v_and_or_b32 v7, v7, s3, v16
	s_waitcnt vmcnt(0)
	v_lshrrev_b32_e32 v9, 9, v200
	v_and_or_b32 v8, v8, s3, v18
	v_and_or_b32 v9, v9, s3, v20
	ds_write_b128 v204, v[6:9] offset:48
	v_pk_mul_f32 v[0:1], v[2:3], v[10:11] op_sel_hi:[1,0]
	v_pk_mul_f32 v[2:3], v[4:5], v[10:11] op_sel_hi:[1,0]
	v_mul_f32_e32 v0, v0, v195
	v_mul_f32_e32 v1, v1, v197
	v_mul_f32_e32 v2, v2, v199
	v_mul_f32_e32 v3, v3, v201
	ds_write_b128 v204, v[0:3] offset:4144
	s_waitcnt lgkmcnt(0)
	ds_read_b128 v[140:143], v205
	ds_read_b128 v[144:147], v205 offset:1024
	ds_read_b128 v[148:151], v205 offset:2048
	ds_read_b128 v[152:155], v205 offset:3072
	ds_read_b128 v[156:159], v205 offset:4096
	ds_read_b128 v[160:163], v205 offset:5120
	ds_read_b128 v[164:167], v205 offset:6144
	ds_read_b128 v[206:209], v205 offset:7168
	s_waitcnt lgkmcnt(0)
	global_store_dwordx4 v203, v[140:143], s[98:99] sc0 sc1
	global_store_dwordx4 v203, v[144:147], s[98:99] offset:1024 sc0 sc1
	global_store_dwordx4 v203, v[148:151], s[98:99] offset:2048 sc0 sc1
	global_store_dwordx4 v203, v[152:155], s[98:99] offset:3072 sc0 sc1
	global_store_dwordx4 v203, v[156:159], s[100:101] sc0 sc1
	global_store_dwordx4 v203, v[160:163], s[100:101] offset:1024 sc0 sc1
	global_store_dwordx4 v203, v[164:167], s[100:101] offset:2048 sc0 sc1
	global_store_dwordx4 v203, v[206:209], s[100:101] offset:3072 sc0 sc1
